# speedup vs baseline: 1.0049x; 1.0049x over previous
_Z9ssim_mainPKfS0_S0_Pf:
	v_readfirstlane_b32 s29, v0
	v_cmp_gt_u32_e32 vcc, 32, v0
	s_nop 1
	s_and_saveexec_b64 s[30:31], vcc
	v_mov_b32_e32 v1, 0x10000
	v_lshl_or_b32 v1, v0, 2, v1
	v_mov_b32_e32 v2, 0
	ds_write_b32 v1, v2
	s_or_b64 exec, exec, s[30:31]
	s_load_dwordx4 s[4:7], s[0:1], 0x0
	s_load_dwordx4 s[8:11], s[0:1], 0x10
	s_lshr_b32 s12, s29, 6
	s_mov_b32 s51, 0x44800000
	s_mov_b32 s38, 0
	s_mov_b32 s39, -1
	v_and_b32_e32 v1, 63, v0
	v_and_b32_e32 v9, 15, v0
	v_bfe_u32 v164, v0, 4, 2
	v_lshlrev_b32_e32 v167, 3, v164
	v_xor_b32_e32 v168, 16, v167
	v_sub_u32_e32 v165, v167, v9
	v_sub_u32_e32 v166, v168, v9
	v_add_u32_e32 v172, 0, v165
	v_med3_i32 v172, v172, 0, 10
	v_lshlrev_b32_e32 v172, 2, v172
	v_add_u32_e32 v173, 1, v165
	v_med3_i32 v173, v173, 0, 10
	v_lshlrev_b32_e32 v173, 2, v173
	v_add_u32_e32 v174, 2, v165
	v_med3_i32 v174, v174, 0, 10
	v_lshlrev_b32_e32 v174, 2, v174
	v_add_u32_e32 v175, 3, v165
	v_med3_i32 v175, v175, 0, 10
	v_lshlrev_b32_e32 v175, 2, v175
	v_add_u32_e32 v176, 4, v165
	v_med3_i32 v176, v176, 0, 10
	v_lshlrev_b32_e32 v176, 2, v176
	v_add_u32_e32 v177, 5, v165
	v_med3_i32 v177, v177, 0, 10
	v_lshlrev_b32_e32 v177, 2, v177
	v_add_u32_e32 v178, 6, v165
	v_med3_i32 v178, v178, 0, 10
	v_lshlrev_b32_e32 v178, 2, v178
	v_add_u32_e32 v179, 7, v165
	v_med3_i32 v179, v179, 0, 10
	v_lshlrev_b32_e32 v179, 2, v179
	v_add_u32_e32 v180, 0, v166
	v_med3_i32 v180, v180, 0, 10
	v_lshlrev_b32_e32 v180, 2, v180
	v_add_u32_e32 v181, 1, v166
	v_med3_i32 v181, v181, 0, 10
	v_lshlrev_b32_e32 v181, 2, v181
	v_add_u32_e32 v182, 2, v166
	v_med3_i32 v182, v182, 0, 10
	v_lshlrev_b32_e32 v182, 2, v182
	v_add_u32_e32 v183, 3, v166
	v_med3_i32 v183, v183, 0, 10
	v_lshlrev_b32_e32 v183, 2, v183
	v_add_u32_e32 v184, 4, v166
	v_med3_i32 v184, v184, 0, 10
	v_lshlrev_b32_e32 v184, 2, v184
	v_add_u32_e32 v185, 5, v166
	v_med3_i32 v185, v185, 0, 10
	v_lshlrev_b32_e32 v185, 2, v185
	v_add_u32_e32 v186, 6, v166
	v_med3_i32 v186, v186, 0, 10
	v_lshlrev_b32_e32 v186, 2, v186
	v_add_u32_e32 v187, 7, v166
	v_med3_i32 v187, v187, 0, 10
	v_lshlrev_b32_e32 v187, 2, v187
	s_waitcnt lgkmcnt(0)
	global_load_dword v188, v172, s[8:9]
	global_load_dword v189, v173, s[8:9]
	global_load_dword v190, v174, s[8:9]
	global_load_dword v191, v175, s[8:9]
	global_load_dword v192, v176, s[8:9]
	global_load_dword v193, v177, s[8:9]
	global_load_dword v194, v178, s[8:9]
	global_load_dword v195, v179, s[8:9]
	global_load_dword v196, v180, s[8:9]
	global_load_dword v197, v181, s[8:9]
	global_load_dword v198, v182, s[8:9]
	global_load_dword v199, v183, s[8:9]
	global_load_dword v200, v184, s[8:9]
	global_load_dword v201, v185, s[8:9]
	global_load_dword v202, v186, s[8:9]
	global_load_dword v203, v187, s[8:9]
	s_load_dwordx8 s[40:47], s[8:9], 0x0
	s_load_dwordx2 s[48:49], s[8:9], 0x20
	s_load_dword s50, s[8:9], 0x28
	s_and_b32 s13, s2, 7
	s_lshl_b32 s13, s13, 5
	s_lshr_b32 s14, s2, 3
	s_add_u32 s13, s13, s14
	s_lshr_b32 s14, s13, 3
	s_and_b32 s15, s13, 7
	s_lshl_b32 s16, s14, 20
	s_lshl_b32 s17, s15, 17
	s_add_u32 s16, s16, s17
	s_lshl_b32 s17, s12, 8
	s_add_u32 s16, s16, s17
	s_add_u32 s18, s4, s16
	s_addc_u32 s19, s5, 0
	s_add_u32 s20, s6, s16
	s_addc_u32 s21, s7, 0
	s_mov_b32 s52, s18
	s_mov_b32 s53, s19
	s_add_u32 s54, s18, 0x1000
	s_addc_u32 s55, s19, 0
	s_add_u32 s56, s18, 0x2000
	s_addc_u32 s57, s19, 0
	s_add_u32 s58, s18, 0x3000
	s_addc_u32 s59, s19, 0
	s_add_u32 s60, s18, 0x10000
	s_addc_u32 s61, s19, 0
	s_add_u32 s62, s18, 0x11000
	s_addc_u32 s63, s19, 0
	s_add_u32 s64, s18, 0x12000
	s_addc_u32 s65, s19, 0
	s_add_u32 s66, s18, 0x13000
	s_addc_u32 s67, s19, 0
	s_mov_b32 s68, s20
	s_mov_b32 s69, s21
	s_add_u32 s70, s20, 0x1000
	s_addc_u32 s71, s21, 0
	s_add_u32 s72, s20, 0x2000
	s_addc_u32 s73, s21, 0
	s_add_u32 s74, s20, 0x3000
	s_addc_u32 s75, s21, 0
	s_add_u32 s76, s20, 0x10000
	s_addc_u32 s77, s21, 0
	s_add_u32 s78, s20, 0x11000
	s_addc_u32 s79, s21, 0
	s_add_u32 s80, s20, 0x12000
	s_addc_u32 s81, s21, 0
	s_add_u32 s82, s20, 0x13000
	s_addc_u32 s83, s21, 0
	s_cmp_eq_u32 s15, 7
	s_cselect_b32 s22, 0, 0x20000
	s_add_u32 s84, s18, s22
	s_addc_u32 s85, s19, 0
	s_add_u32 s86, s18, s22
	s_addc_u32 s87, s19, 0
	s_add_u32 s86, s86, 0x1000
	s_addc_u32 s87, s87, 0
	s_add_u32 s88, s20, s22
	s_addc_u32 s89, s21, 0
	s_add_u32 s90, s20, s22
	s_addc_u32 s91, s21, 0
	s_add_u32 s90, s90, 0x1000
	s_addc_u32 s91, s91, 0
	v_lshrrev_b32_e32 v167, 2, v9
	v_lshlrev_b32_e32 v167, 5, v167
	v_and_b32_e32 v168, 1, v9
	v_lshl_or_b32 v167, v168, 4, v167
	v_bfe_u32 v168, v9, 1, 1
	v_lshl_or_b32 v167, v168, 7, v167
	v_lshl_or_b32 v2, v164, 14, v167
	v_and_b32_e32 v168, 1, v164
	v_lshl_or_b32 v3, v168, 14, v167
	v_lshrrev_b32_e32 v168, 1, v164
	v_lshl_or_b32 v3, v168, 13, v3
	global_load_dwordx4 v[36:39], v2, s[52:53] offset:0 nt
	global_load_dwordx4 v[40:43], v2, s[52:53] offset:2048 nt
	global_load_dwordx4 v[68:71], v2, s[68:69] offset:0 nt
	global_load_dwordx4 v[72:75], v2, s[68:69] offset:2048 nt
	global_load_dwordx4 v[44:47], v2, s[54:55] offset:0 nt
	global_load_dwordx4 v[48:51], v2, s[54:55] offset:2048 nt
	global_load_dwordx4 v[76:79], v2, s[70:71] offset:0 nt
	global_load_dwordx4 v[80:83], v2, s[70:71] offset:2048 nt
	global_load_dwordx4 v[52:55], v2, s[56:57] offset:0 nt
	global_load_dwordx4 v[56:59], v2, s[56:57] offset:2048 nt
	global_load_dwordx4 v[84:87], v2, s[72:73] offset:0 nt
	global_load_dwordx4 v[88:91], v2, s[72:73] offset:2048 nt
	global_load_dwordx4 v[60:63], v2, s[58:59] offset:0 nt
	global_load_dwordx4 v[64:67], v2, s[58:59] offset:2048 nt
	global_load_dwordx4 v[92:95], v2, s[74:75] offset:0 nt
	global_load_dwordx4 v[96:99], v2, s[74:75] offset:2048 nt
	global_load_dwordx4 v[100:103], v2, s[60:61] offset:0 nt
	global_load_dwordx4 v[104:107], v2, s[60:61] offset:2048 nt
	global_load_dwordx4 v[132:135], v2, s[76:77] offset:0 nt
	global_load_dwordx4 v[136:139], v2, s[76:77] offset:2048 nt
	global_load_dwordx4 v[108:111], v2, s[62:63] offset:0 nt
	global_load_dwordx4 v[112:115], v2, s[62:63] offset:2048 nt
	global_load_dwordx4 v[140:143], v2, s[78:79] offset:0 nt
	global_load_dwordx4 v[144:147], v2, s[78:79] offset:2048 nt
	global_load_dwordx4 v[116:119], v2, s[64:65] offset:0 nt
	global_load_dwordx4 v[120:123], v2, s[64:65] offset:2048 nt
	global_load_dwordx4 v[148:151], v2, s[80:81] offset:0 nt
	global_load_dwordx4 v[152:155], v2, s[80:81] offset:2048 nt
	global_load_dwordx4 v[124:127], v2, s[66:67] offset:0 nt
	global_load_dwordx4 v[128:131], v2, s[66:67] offset:2048 nt
	global_load_dwordx4 v[156:159], v2, s[82:83] offset:0 nt
	global_load_dwordx4 v[160:163], v2, s[82:83] offset:2048 nt
	s_waitcnt vmcnt(32)
	v_cmp_lt_u32_e64 s[32:33], 31, v1
	v_cmp_gt_u32_e64 s[34:35], 32, v1
	v_fma_mixlo_f16 v204, v188, s51, 0
	v_add_u32_e32 v167, 0, v165
	v_cmp_gt_u32_e32 vcc, 11, v167
	s_nop 1
	v_cndmask_b32_e32 v204, 0, v204, vcc
	v_fma_mixlo_f16 v205, v189, s51, 0
	v_add_u32_e32 v167, 1, v165
	v_cmp_gt_u32_e32 vcc, 11, v167
	s_nop 1
	v_cndmask_b32_e32 v205, 0, v205, vcc
	v_fma_mixlo_f16 v206, v190, s51, 0
	v_add_u32_e32 v167, 2, v165
	v_cmp_gt_u32_e32 vcc, 11, v167
	s_nop 1
	v_cndmask_b32_e32 v206, 0, v206, vcc
	v_fma_mixlo_f16 v207, v191, s51, 0
	v_add_u32_e32 v167, 3, v165
	v_cmp_gt_u32_e32 vcc, 11, v167
	s_nop 1
	v_cndmask_b32_e32 v207, 0, v207, vcc
	v_fma_mixlo_f16 v208, v192, s51, 0
	v_add_u32_e32 v167, 4, v165
	v_cmp_gt_u32_e32 vcc, 11, v167
	s_nop 1
	v_cndmask_b32_e32 v208, 0, v208, vcc
	v_fma_mixlo_f16 v209, v193, s51, 0
	v_add_u32_e32 v167, 5, v165
	v_cmp_gt_u32_e32 vcc, 11, v167
	s_nop 1
	v_cndmask_b32_e32 v209, 0, v209, vcc
	v_fma_mixlo_f16 v210, v194, s51, 0
	v_add_u32_e32 v167, 6, v165
	v_cmp_gt_u32_e32 vcc, 11, v167
	s_nop 1
	v_cndmask_b32_e32 v210, 0, v210, vcc
	v_fma_mixlo_f16 v211, v195, s51, 0
	v_add_u32_e32 v167, 7, v165
	v_cmp_gt_u32_e32 vcc, 11, v167
	s_nop 1
	v_cndmask_b32_e32 v211, 0, v211, vcc
	v_pack_b32_f16 v24, v204, v205
	v_pack_b32_f16 v25, v206, v207
	v_pack_b32_f16 v26, v208, v209
	v_pack_b32_f16 v27, v210, v211
	v_fma_mixlo_f16 v204, v196, s51, 0
	v_add_u32_e32 v167, 0, v166
	v_cmp_gt_u32_e32 vcc, 11, v167
	s_nop 1
	v_cndmask_b32_e32 v204, 0, v204, vcc
	v_fma_mixlo_f16 v205, v197, s51, 0
	v_add_u32_e32 v167, 1, v166
	v_cmp_gt_u32_e32 vcc, 11, v167
	s_nop 1
	v_cndmask_b32_e32 v205, 0, v205, vcc
	v_fma_mixlo_f16 v206, v198, s51, 0
	v_add_u32_e32 v167, 2, v166
	v_cmp_gt_u32_e32 vcc, 11, v167
	s_nop 1
	v_cndmask_b32_e32 v206, 0, v206, vcc
	v_fma_mixlo_f16 v207, v199, s51, 0
	v_add_u32_e32 v167, 3, v166
	v_cmp_gt_u32_e32 vcc, 11, v167
	s_nop 1
	v_cndmask_b32_e32 v207, 0, v207, vcc
	v_fma_mixlo_f16 v208, v200, s51, 0
	v_add_u32_e32 v167, 4, v166
	v_cmp_gt_u32_e32 vcc, 11, v167
	s_nop 1
	v_cndmask_b32_e32 v208, 0, v208, vcc
	v_fma_mixlo_f16 v209, v201, s51, 0
	v_add_u32_e32 v167, 5, v166
	v_cmp_gt_u32_e32 vcc, 11, v167
	s_nop 1
	v_cndmask_b32_e32 v209, 0, v209, vcc
	v_fma_mixlo_f16 v210, v202, s51, 0
	v_add_u32_e32 v167, 6, v166
	v_cmp_gt_u32_e32 vcc, 11, v167
	s_nop 1
	v_cndmask_b32_e32 v210, 0, v210, vcc
	v_fma_mixlo_f16 v211, v203, s51, 0
	v_add_u32_e32 v167, 7, v166
	v_cmp_gt_u32_e32 vcc, 11, v167
	s_nop 1
	v_cndmask_b32_e32 v211, 0, v211, vcc
	v_pack_b32_f16 v167, v204, v205
	v_cndmask_b32_e64 v28, 0, v167, s[32:33]
	v_cndmask_b32_e64 v32, 0, v167, s[34:35]
	v_pack_b32_f16 v167, v206, v207
	v_cndmask_b32_e64 v29, 0, v167, s[32:33]
	v_cndmask_b32_e64 v33, 0, v167, s[34:35]
	v_pack_b32_f16 v167, v208, v209
	v_cndmask_b32_e64 v30, 0, v167, s[32:33]
	v_cndmask_b32_e64 v34, 0, v167, s[34:35]
	v_pack_b32_f16 v167, v210, v211
	v_cndmask_b32_e64 v31, 0, v167, s[32:33]
	v_cndmask_b32_e64 v35, 0, v167, s[34:35]
	s_waitcnt lgkmcnt(0)
	v_mov_b32_e32 v229, 0x44800000
	v_fma_mixlo_f16 v228, s40, v229, 0
	v_cvt_f32_f16_e32 v228, v228
	v_cvt_f64_f32_e32 v[212:213], v228
	v_add_f64 v[212:213], v[212:213], 0
	v_fma_mixlo_f16 v228, s41, v229, 0
	v_cvt_f32_f16_e32 v228, v228
	v_cvt_f64_f32_e32 v[214:215], v228
	v_add_f64 v[212:213], v[212:213], v[214:215]
	v_fma_mixlo_f16 v228, s42, v229, 0
	v_cvt_f32_f16_e32 v228, v228
	v_cvt_f64_f32_e32 v[214:215], v228
	v_add_f64 v[212:213], v[212:213], v[214:215]
	v_fma_mixlo_f16 v228, s43, v229, 0
	v_cvt_f32_f16_e32 v228, v228
	v_cvt_f64_f32_e32 v[214:215], v228
	v_add_f64 v[212:213], v[212:213], v[214:215]
	v_fma_mixlo_f16 v228, s44, v229, 0
	v_cvt_f32_f16_e32 v228, v228
	v_cvt_f64_f32_e32 v[214:215], v228
	v_add_f64 v[212:213], v[212:213], v[214:215]
	v_fma_mixlo_f16 v228, s45, v229, 0
	v_cvt_f32_f16_e32 v228, v228
	v_cvt_f64_f32_e32 v[214:215], v228
	v_add_f64 v[212:213], v[212:213], v[214:215]
	v_fma_mixlo_f16 v228, s46, v229, 0
	v_cvt_f32_f16_e32 v228, v228
	v_cvt_f64_f32_e32 v[214:215], v228
	v_add_f64 v[212:213], v[212:213], v[214:215]
	v_fma_mixlo_f16 v228, s47, v229, 0
	v_cvt_f32_f16_e32 v228, v228
	v_cvt_f64_f32_e32 v[214:215], v228
	v_add_f64 v[212:213], v[212:213], v[214:215]
	v_fma_mixlo_f16 v228, s48, v229, 0
	v_cvt_f32_f16_e32 v228, v228
	v_cvt_f64_f32_e32 v[214:215], v228
	v_add_f64 v[212:213], v[212:213], v[214:215]
	v_fma_mixlo_f16 v228, s49, v229, 0
	v_cvt_f32_f16_e32 v228, v228
	v_cvt_f64_f32_e32 v[214:215], v228
	v_add_f64 v[212:213], v[212:213], v[214:215]
	v_fma_mixlo_f16 v228, s50, v229, 0
	v_cvt_f32_f16_e32 v228, v228
	v_cvt_f64_f32_e32 v[214:215], v228
	v_add_f64 v[212:213], v[212:213], v[214:215]
	v_mul_f64 v[212:213], v[212:213], v[212:213]
	v_mul_f64 v[216:217], v[212:213], 0.5
	v_add_f64 v[218:219], v[216:217], v[216:217]
	s_mov_b32 s36, 0xeb1c432d
	s_mov_b32 s37, 0x3f1a36e2
	v_mul_f64 v[220:221], v[212:213], s[36:37]
	v_mul_f64 v[222:223], v[216:217], v[218:219]
	v_fmac_f64_e32 v[222:223], v[212:213], v[220:221]
	v_add_f64 v[224:225], v[212:213], v[212:213]
	s_mov_b32 s36, 0x487fcb92
	s_mov_b32 s37, 0x3f4d7dbf
	v_mul_f64 v[226:227], v[212:213], s[36:37]
	v_cvt_f32_f64_e32 v10, v[218:219]
	v_cvt_f32_f64_e32 v11, v[222:223]
	v_cvt_f32_f64_e32 v12, v[212:213]
	v_cvt_f32_f64_e32 v13, v[224:225]
	v_mul_f64 v[226:227], v[212:213], v[226:227]
	v_cvt_f32_f64_e32 v14, v[226:227]
	v_lshlrev_b32_e32 v167, 2, v164
	s_cmp_eq_u32 s12, 0
	s_cselect_b32 s23, 6, 64
	v_add_u32_e32 v168, 0, v167
	v_cmp_gt_u32_e32 vcc, s23, v168
	s_nop 1
	v_cndmask_b32_e64 v15, 0, 1.0, vcc
	v_add_u32_e32 v168, 1, v167
	v_cmp_gt_u32_e32 vcc, s23, v168
	s_nop 1
	v_cndmask_b32_e64 v16, 0, 1.0, vcc
	v_add_u32_e32 v168, 2, v167
	v_cmp_gt_u32_e32 vcc, s23, v168
	s_nop 1
	v_cndmask_b32_e64 v17, 0, 1.0, vcc
	v_add_u32_e32 v168, 3, v167
	v_cmp_gt_u32_e32 vcc, s23, v168
	s_nop 1
	v_cndmask_b32_e64 v18, 0, 1.0, vcc
	v_and_b32_e32 v167, 31, v1
	v_lshlrev_b32_e32 v167, 4, v167
	s_lshl_b32 s24, s12, 11
	s_add_i32 s25, s12, 7
	s_and_b32 s25, s25, 7
	s_lshl_b32 s26, s25, 11
	v_or_b32_e32 v4, s24, v167
	v_or_b32_e32 v5, s26, v167
	s_lshl_b32 s27, s12, 2
	s_add_u32 s27, s27, 0x10000
	s_lshl_b32 s28, s25, 2
	s_add_u32 s28, s28, 0x10000
	v_mov_b32_e32 v6, s27
	v_mov_b32_e32 v7, s28
	v_mov_b32_e32 v8, 1
	v_mov_b32_e32 v19, 0
	v_mov_b32_e32 v20, 0
	v_mov_b32_e32 v21, 0
	v_mov_b32_e32 v22, 0
	s_waitcnt lgkmcnt(0)
	s_barrier
	s_waitcnt vmcnt(28)
	v_cvt_pk_f16_f32 v164, v36, v40
	v_cvt_pk_f16_f32 v180, v68, v72
	v_pk_add_f16 v164, v164, -0.5 op_sel_hi:[1,0]
	v_pk_add_f16 v180, v180, -0.5 op_sel_hi:[1,0]
	v_pk_mul_f16 v196, v180, v180
	v_pk_mul_f16 v212, v164, v180
	v_pk_fma_f16 v196, v164, v164, v196
	v_cvt_pk_f16_f32 v168, v37, v41
	v_cvt_pk_f16_f32 v184, v69, v73
	v_pk_add_f16 v168, v168, -0.5 op_sel_hi:[1,0]
	v_pk_add_f16 v184, v184, -0.5 op_sel_hi:[1,0]
	v_pk_mul_f16 v200, v184, v184
	v_pk_mul_f16 v216, v168, v184
	v_pk_fma_f16 v200, v168, v168, v200
	v_cvt_pk_f16_f32 v172, v38, v42
	v_cvt_pk_f16_f32 v188, v70, v74
	v_pk_add_f16 v172, v172, -0.5 op_sel_hi:[1,0]
	v_pk_add_f16 v188, v188, -0.5 op_sel_hi:[1,0]
	v_pk_mul_f16 v204, v188, v188
	v_pk_mul_f16 v220, v172, v188
	v_pk_fma_f16 v204, v172, v172, v204
	v_cvt_pk_f16_f32 v176, v39, v43
	v_cvt_pk_f16_f32 v192, v71, v75
	v_pk_add_f16 v176, v176, -0.5 op_sel_hi:[1,0]
	v_pk_add_f16 v192, v192, -0.5 op_sel_hi:[1,0]
	v_pk_mul_f16 v208, v192, v192
	v_pk_mul_f16 v224, v176, v192
	v_pk_fma_f16 v208, v176, v176, v208
	s_waitcnt vmcnt(24)
	v_cvt_pk_f16_f32 v165, v44, v48
	v_cvt_pk_f16_f32 v181, v76, v80
	v_pk_add_f16 v165, v165, -0.5 op_sel_hi:[1,0]
	v_pk_add_f16 v181, v181, -0.5 op_sel_hi:[1,0]
	v_pk_mul_f16 v197, v181, v181
	v_pk_mul_f16 v213, v165, v181
	v_pk_fma_f16 v197, v165, v165, v197
	v_cvt_pk_f16_f32 v169, v45, v49
	v_cvt_pk_f16_f32 v185, v77, v81
	v_pk_add_f16 v169, v169, -0.5 op_sel_hi:[1,0]
	v_pk_add_f16 v185, v185, -0.5 op_sel_hi:[1,0]
	v_pk_mul_f16 v201, v185, v185
	v_pk_mul_f16 v217, v169, v185
	v_pk_fma_f16 v201, v169, v169, v201
	v_cvt_pk_f16_f32 v173, v46, v50
	v_cvt_pk_f16_f32 v189, v78, v82
	v_pk_add_f16 v173, v173, -0.5 op_sel_hi:[1,0]
	v_pk_add_f16 v189, v189, -0.5 op_sel_hi:[1,0]
	v_pk_mul_f16 v205, v189, v189
	v_pk_mul_f16 v221, v173, v189
	v_pk_fma_f16 v205, v173, v173, v205
	v_cvt_pk_f16_f32 v177, v47, v51
	v_cvt_pk_f16_f32 v193, v79, v83
	v_pk_add_f16 v177, v177, -0.5 op_sel_hi:[1,0]
	v_pk_add_f16 v193, v193, -0.5 op_sel_hi:[1,0]
	v_pk_mul_f16 v209, v193, v193
	v_pk_mul_f16 v225, v177, v193
	v_pk_fma_f16 v209, v177, v177, v209
	s_waitcnt vmcnt(20)
	v_cvt_pk_f16_f32 v166, v52, v56
	v_cvt_pk_f16_f32 v182, v84, v88
	v_pk_add_f16 v166, v166, -0.5 op_sel_hi:[1,0]
	v_pk_add_f16 v182, v182, -0.5 op_sel_hi:[1,0]
	v_pk_mul_f16 v198, v182, v182
	v_pk_mul_f16 v214, v166, v182
	v_pk_fma_f16 v198, v166, v166, v198
	v_cvt_pk_f16_f32 v170, v53, v57
	v_cvt_pk_f16_f32 v186, v85, v89
	v_pk_add_f16 v170, v170, -0.5 op_sel_hi:[1,0]
	v_pk_add_f16 v186, v186, -0.5 op_sel_hi:[1,0]
	v_pk_mul_f16 v202, v186, v186
	v_pk_mul_f16 v218, v170, v186
	v_pk_fma_f16 v202, v170, v170, v202
	v_cvt_pk_f16_f32 v174, v54, v58
	v_cvt_pk_f16_f32 v190, v86, v90
	v_pk_add_f16 v174, v174, -0.5 op_sel_hi:[1,0]
	v_pk_add_f16 v190, v190, -0.5 op_sel_hi:[1,0]
	v_pk_mul_f16 v206, v190, v190
	v_pk_mul_f16 v222, v174, v190
	v_pk_fma_f16 v206, v174, v174, v206
	v_cvt_pk_f16_f32 v178, v55, v59
	v_cvt_pk_f16_f32 v194, v87, v91
	v_pk_add_f16 v178, v178, -0.5 op_sel_hi:[1,0]
	v_pk_add_f16 v194, v194, -0.5 op_sel_hi:[1,0]
	v_pk_mul_f16 v210, v194, v194
	v_pk_mul_f16 v226, v178, v194
	v_pk_fma_f16 v210, v178, v178, v210
	s_waitcnt vmcnt(16)
	v_cvt_pk_f16_f32 v167, v60, v64
	v_cvt_pk_f16_f32 v183, v92, v96
	v_pk_add_f16 v167, v167, -0.5 op_sel_hi:[1,0]
	v_pk_add_f16 v183, v183, -0.5 op_sel_hi:[1,0]
	v_pk_mul_f16 v199, v183, v183
	v_pk_mul_f16 v215, v167, v183
	v_pk_fma_f16 v199, v167, v167, v199
	v_cvt_pk_f16_f32 v171, v61, v65
	v_cvt_pk_f16_f32 v187, v93, v97
	v_pk_add_f16 v171, v171, -0.5 op_sel_hi:[1,0]
	v_pk_add_f16 v187, v187, -0.5 op_sel_hi:[1,0]
	v_pk_mul_f16 v203, v187, v187
	v_pk_mul_f16 v219, v171, v187
	v_pk_fma_f16 v203, v171, v171, v203
	v_cvt_pk_f16_f32 v175, v62, v66
	v_cvt_pk_f16_f32 v191, v94, v98
	v_pk_add_f16 v175, v175, -0.5 op_sel_hi:[1,0]
	v_pk_add_f16 v191, v191, -0.5 op_sel_hi:[1,0]
	v_pk_mul_f16 v207, v191, v191
	v_pk_mul_f16 v223, v175, v191
	v_pk_fma_f16 v207, v175, v175, v207
	v_cvt_pk_f16_f32 v179, v63, v67
	v_cvt_pk_f16_f32 v195, v95, v99
	v_pk_add_f16 v179, v179, -0.5 op_sel_hi:[1,0]
	v_pk_add_f16 v195, v195, -0.5 op_sel_hi:[1,0]
	v_pk_mul_f16 v211, v195, v195
	v_pk_mul_f16 v227, v179, v195
	v_pk_fma_f16 v211, v179, v179, v211
	v_mfma_f32_16x16x32_f16 v[68:71], v[164:167], v[24:27], 0
	v_mfma_f32_16x16x32_f16 v[72:75], v[168:171], v[24:27], 0
	v_mfma_f32_16x16x32_f16 v[76:79], v[172:175], v[24:27], 0
	v_mfma_f32_16x16x32_f16 v[80:83], v[176:179], v[24:27], 0
	v_mfma_f32_16x16x32_f16 v[84:87], v[180:183], v[24:27], 0
	v_mfma_f32_16x16x32_f16 v[88:91], v[184:187], v[24:27], 0
	v_mfma_f32_16x16x32_f16 v[92:95], v[188:191], v[24:27], 0
	v_mfma_f32_16x16x32_f16 v[96:99], v[192:195], v[24:27], 0
	s_nop 1
	v_cvt_pk_f16_f32 v36, v68, v72
	s_nop 0
	v_cvt_pk_f16_f32 v37, v76, v80
	v_cvt_pk_f16_f32 v38, v69, v73
	v_cvt_pk_f16_f32 v39, v77, v81
	v_cvt_pk_f16_f32 v40, v70, v74
	v_cvt_pk_f16_f32 v41, v78, v82
	v_cvt_pk_f16_f32 v42, v71, v75
	v_cvt_pk_f16_f32 v43, v79, v83
	v_mfma_f32_16x16x32_f16 v[68:71], v[196:199], v[24:27], 0
	v_mfma_f32_16x16x32_f16 v[72:75], v[200:203], v[24:27], 0
	v_mfma_f32_16x16x32_f16 v[76:79], v[204:207], v[24:27], 0
	v_mfma_f32_16x16x32_f16 v[80:83], v[208:211], v[24:27], 0
	v_cvt_pk_f16_f32 v44, v84, v88
	v_cvt_pk_f16_f32 v45, v92, v96
	v_cvt_pk_f16_f32 v46, v85, v89
	v_cvt_pk_f16_f32 v47, v93, v97
	v_cvt_pk_f16_f32 v48, v86, v90
	v_cvt_pk_f16_f32 v49, v94, v98
	v_cvt_pk_f16_f32 v50, v87, v91
	v_cvt_pk_f16_f32 v51, v95, v99
	v_mfma_f32_16x16x32_f16 v[84:87], v[212:215], v[24:27], 0
	v_mfma_f32_16x16x32_f16 v[88:91], v[216:219], v[24:27], 0
	v_mfma_f32_16x16x32_f16 v[92:95], v[220:223], v[24:27], 0
	v_mfma_f32_16x16x32_f16 v[96:99], v[224:227], v[24:27], 0
	v_cvt_pk_f16_f32 v52, v68, v72
	v_cvt_pk_f16_f32 v53, v76, v80
	v_cvt_pk_f16_f32 v54, v69, v73
	v_cvt_pk_f16_f32 v55, v77, v81
	v_cvt_pk_f16_f32 v56, v70, v74
	v_cvt_pk_f16_f32 v57, v78, v82
	v_cvt_pk_f16_f32 v58, v71, v75
	v_cvt_pk_f16_f32 v59, v79, v83
	v_cvt_pk_f16_f32 v60, v84, v88
	v_cvt_pk_f16_f32 v61, v92, v96
	v_cvt_pk_f16_f32 v62, v85, v89
	v_cvt_pk_f16_f32 v63, v93, v97
	v_cvt_pk_f16_f32 v64, v86, v90
	v_cvt_pk_f16_f32 v65, v94, v98
	v_cvt_pk_f16_f32 v66, v87, v91
	v_cvt_pk_f16_f32 v67, v95, v99
	s_mov_b64 exec, s[38:39]
	ds_write_b128 v4, v[40:43] offset:0
	ds_write_b128 v4, v[48:51] offset:512
	ds_write_b128 v4, v[56:59] offset:1024
	ds_write_b128 v4, v[64:67] offset:1536
	s_mov_b64 exec, -1
	s_waitcnt lgkmcnt(0)
	ds_write_b32 v6, v8 offset:0
	v_mfma_f32_16x16x32_f16 v[68:71], v[24:27], v[36:39], 0
	v_mfma_f32_16x16x32_f16 v[72:75], v[24:27], v[44:47], 0
	v_mfma_f32_16x16x32_f16 v[76:79], v[24:27], v[52:55], 0
	v_mfma_f32_16x16x32_f16 v[80:83], v[24:27], v[60:63], 0
	v_mfma_f32_16x16x32_f16 v[84:87], v[28:31], v[36:39], 0
	v_mfma_f32_16x16x32_f16 v[88:91], v[28:31], v[44:47], 0
	v_mfma_f32_16x16x32_f16 v[92:95], v[28:31], v[52:55], 0
	v_mfma_f32_16x16x32_f16 v[96:99], v[28:31], v[60:63], 0
	v_mfma_f32_16x16x32_f16 v[84:87], v[32:35], v[40:43], v[84:87]
	v_mfma_f32_16x16x32_f16 v[88:91], v[32:35], v[48:51], v[88:91]
	v_mfma_f32_16x16x32_f16 v[92:95], v[32:35], v[56:59], v[92:95]
	v_mfma_f32_16x16x32_f16 v[96:99], v[32:35], v[64:67], v[96:99]
	v_mul_f32_e32 v244, v68, v72
	v_mul_f32_e32 v250, v69, v73
	v_mul_f32_e32 v245, v72, v72
	v_mul_f32_e32 v251, v73, v73
	v_add_f32_e32 v246, v68, v72
	v_add_f32_e32 v252, v69, v73
	v_fma_f32 v245, v68, v68, v245
	v_fma_f32 v251, v69, v69, v251
	v_fma_f32 v247, v10, v246, v11
	v_fma_f32 v253, v10, v252, v11
	v_fma_f32 v246, v13, v80, v14
	v_fma_f32 v252, v13, v81, v14
	v_fma_f32 v248, v12, v76, v14
	v_fma_f32 v254, v12, v77, v14
	v_fma_f32 v249, 2.0, v244, v247
	v_fma_f32 v255, 2.0, v250, v253
	v_add_f32_e32 v247, v245, v247
	v_add_f32_e32 v253, v251, v253
	v_fma_f32 v246, -2.0, v244, v246
	v_fma_f32 v252, -2.0, v250, v252
	v_sub_f32_e32 v248, v248, v245
	v_sub_f32_e32 v254, v254, v251
	v_mul_f32_e32 v247, v247, v248
	v_mul_f32_e32 v253, v253, v254
	v_rcp_f32_e32 v247, v247
	v_rcp_f32_e32 v253, v253
	v_mul_f32_e32 v249, v249, v246
	v_mul_f32_e32 v255, v255, v252
	v_mul_f32_e32 v249, v249, v247
	v_mul_f32_e32 v255, v255, v253
	v_add_f32_e32 v19, v19, v249
	v_add_f32_e32 v19, v19, v255
	v_mul_f32_e32 v244, v70, v74
	v_mul_f32_e32 v250, v71, v75
	v_mul_f32_e32 v245, v74, v74
	v_mul_f32_e32 v251, v75, v75
	v_add_f32_e32 v246, v70, v74
	v_add_f32_e32 v252, v71, v75
	v_fma_f32 v245, v70, v70, v245
	v_fma_f32 v251, v71, v71, v251
	v_fma_f32 v247, v10, v246, v11
	v_fma_f32 v253, v10, v252, v11
	v_fma_f32 v246, v13, v82, v14
	v_fma_f32 v252, v13, v83, v14
	v_fma_f32 v248, v12, v78, v14
	v_fma_f32 v254, v12, v79, v14
	v_fma_f32 v249, 2.0, v244, v247
	v_fma_f32 v255, 2.0, v250, v253
	v_add_f32_e32 v247, v245, v247
	v_add_f32_e32 v253, v251, v253
	v_fma_f32 v246, -2.0, v244, v246
	v_fma_f32 v252, -2.0, v250, v252
	v_sub_f32_e32 v248, v248, v245
	v_sub_f32_e32 v254, v254, v251
	v_mul_f32_e32 v247, v247, v248
	v_mul_f32_e32 v253, v253, v254
	v_rcp_f32_e32 v247, v247
	v_rcp_f32_e32 v253, v253
	v_mul_f32_e32 v249, v249, v246
	v_mul_f32_e32 v255, v255, v252
	v_mul_f32_e32 v249, v249, v247
	v_mul_f32_e32 v255, v255, v253
	v_add_f32_e32 v20, v20, v249
	v_add_f32_e32 v20, v20, v255
	v_mfma_f32_16x16x32_f16 v[68:71], v[24:27], v[40:43], 0
	v_mfma_f32_16x16x32_f16 v[72:75], v[24:27], v[48:51], 0
	v_mfma_f32_16x16x32_f16 v[76:79], v[24:27], v[56:59], 0
	v_mfma_f32_16x16x32_f16 v[80:83], v[24:27], v[64:67], 0
	ds_read_b32 v23, v7 offset:0
	s_waitcnt lgkmcnt(0)
	v_cmp_ne_u32_e32 vcc, 0, v23
	s_cbranch_vccnz .Lq_go_0
.Lq_spin_0:
	s_sleep 1
	ds_read_b32 v23, v7 offset:0
	s_waitcnt lgkmcnt(0)
	v_cmp_eq_u32_e32 vcc, 0, v23
	s_cbranch_vccnz .Lq_spin_0
.Lq_go_0:
	ds_read_b128 v[228:231], v5 offset:0
	ds_read_b128 v[232:235], v5 offset:512
	ds_read_b128 v[236:239], v5 offset:1024
	ds_read_b128 v[240:243], v5 offset:1536
	v_mul_f32_e32 v244, v84, v88
	v_mul_f32_e32 v250, v85, v89
	v_mul_f32_e32 v245, v88, v88
	v_mul_f32_e32 v251, v89, v89
	v_add_f32_e32 v246, v84, v88
	v_add_f32_e32 v252, v85, v89
	v_fma_f32 v245, v84, v84, v245
	v_fma_f32 v251, v85, v85, v251
	v_fma_f32 v247, v10, v246, v11
	v_fma_f32 v253, v10, v252, v11
	v_fma_f32 v246, v13, v96, v14
	v_fma_f32 v252, v13, v97, v14
	v_fma_f32 v248, v12, v92, v14
	v_fma_f32 v254, v12, v93, v14
	v_fma_f32 v249, 2.0, v244, v247
	v_fma_f32 v255, 2.0, v250, v253
	v_add_f32_e32 v247, v245, v247
	v_add_f32_e32 v253, v251, v253
	v_fma_f32 v246, -2.0, v244, v246
	v_fma_f32 v252, -2.0, v250, v252
	v_sub_f32_e32 v248, v248, v245
	v_sub_f32_e32 v254, v254, v251
	v_mul_f32_e32 v247, v247, v248
	v_mul_f32_e32 v253, v253, v254
	v_rcp_f32_e32 v247, v247
	v_rcp_f32_e32 v253, v253
	v_mul_f32_e32 v249, v249, v246
	v_mul_f32_e32 v255, v255, v252
	v_mul_f32_e32 v249, v249, v247
	v_mul_f32_e32 v255, v255, v253
	v_add_f32_e32 v19, v19, v249
	v_add_f32_e32 v19, v19, v255
	v_mul_f32_e32 v244, v86, v90
	v_mul_f32_e32 v250, v87, v91
	v_mul_f32_e32 v245, v90, v90
	v_mul_f32_e32 v251, v91, v91
	v_add_f32_e32 v246, v86, v90
	v_add_f32_e32 v252, v87, v91
	v_fma_f32 v245, v86, v86, v245
	v_fma_f32 v251, v87, v87, v251
	v_fma_f32 v247, v10, v246, v11
	v_fma_f32 v253, v10, v252, v11
	v_fma_f32 v246, v13, v98, v14
	v_fma_f32 v252, v13, v99, v14
	v_fma_f32 v248, v12, v94, v14
	v_fma_f32 v254, v12, v95, v14
	v_fma_f32 v249, 2.0, v244, v247
	v_fma_f32 v255, 2.0, v250, v253
	v_add_f32_e32 v247, v245, v247
	v_add_f32_e32 v253, v251, v253
	v_fma_f32 v246, -2.0, v244, v246
	v_fma_f32 v252, -2.0, v250, v252
	v_sub_f32_e32 v248, v248, v245
	v_sub_f32_e32 v254, v254, v251
	v_mul_f32_e32 v247, v247, v248
	v_mul_f32_e32 v253, v253, v254
	v_rcp_f32_e32 v247, v247
	v_rcp_f32_e32 v253, v253
	v_mul_f32_e32 v249, v249, v246
	v_mul_f32_e32 v255, v255, v252
	v_mul_f32_e32 v249, v249, v247
	v_mul_f32_e32 v255, v255, v253
	v_add_f32_e32 v20, v20, v249
	v_add_f32_e32 v20, v20, v255
	s_waitcnt lgkmcnt(0)
	v_mfma_f32_16x16x32_f16 v[84:87], v[28:31], v[228:231], 0
	v_mfma_f32_16x16x32_f16 v[88:91], v[28:31], v[232:235], 0
	v_mfma_f32_16x16x32_f16 v[92:95], v[28:31], v[236:239], 0
	v_mfma_f32_16x16x32_f16 v[96:99], v[28:31], v[240:243], 0
	v_mfma_f32_16x16x32_f16 v[84:87], v[32:35], v[36:39], v[84:87]
	v_mfma_f32_16x16x32_f16 v[88:91], v[32:35], v[44:47], v[88:91]
	v_mfma_f32_16x16x32_f16 v[92:95], v[32:35], v[52:55], v[92:95]
	v_mfma_f32_16x16x32_f16 v[96:99], v[32:35], v[60:63], v[96:99]
	v_mul_f32_e32 v244, v68, v72
	v_mul_f32_e32 v250, v69, v73
	v_mul_f32_e32 v245, v72, v72
	v_mul_f32_e32 v251, v73, v73
	v_add_f32_e32 v246, v68, v72
	v_add_f32_e32 v252, v69, v73
	v_fma_f32 v245, v68, v68, v245
	v_fma_f32 v251, v69, v69, v251
	v_fma_f32 v247, v10, v246, v11
	v_fma_f32 v253, v10, v252, v11
	v_fma_f32 v246, v13, v80, v14
	v_fma_f32 v252, v13, v81, v14
	v_fma_f32 v248, v12, v76, v14
	v_fma_f32 v254, v12, v77, v14
	v_fma_f32 v249, 2.0, v244, v247
	v_fma_f32 v255, 2.0, v250, v253
	v_add_f32_e32 v247, v245, v247
	v_add_f32_e32 v253, v251, v253
	v_fma_f32 v246, -2.0, v244, v246
	v_fma_f32 v252, -2.0, v250, v252
	v_sub_f32_e32 v248, v248, v245
	v_sub_f32_e32 v254, v254, v251
	v_mul_f32_e32 v247, v247, v248
	v_mul_f32_e32 v253, v253, v254
	v_rcp_f32_e32 v247, v247
	v_rcp_f32_e32 v253, v253
	v_mul_f32_e32 v249, v249, v246
	v_mul_f32_e32 v255, v255, v252
	v_mul_f32_e32 v249, v249, v247
	v_mul_f32_e32 v255, v255, v253
	v_add_f32_e32 v19, v19, v249
	v_add_f32_e32 v19, v19, v255
	v_mul_f32_e32 v244, v70, v74
	v_mul_f32_e32 v250, v71, v75
	v_mul_f32_e32 v245, v74, v74
	v_mul_f32_e32 v251, v75, v75
	v_add_f32_e32 v246, v70, v74
	v_add_f32_e32 v252, v71, v75
	v_fma_f32 v245, v70, v70, v245
	v_fma_f32 v251, v71, v71, v251
	v_fma_f32 v247, v10, v246, v11
	v_fma_f32 v253, v10, v252, v11
	v_fma_f32 v246, v13, v82, v14
	v_fma_f32 v252, v13, v83, v14
	v_fma_f32 v248, v12, v78, v14
	v_fma_f32 v254, v12, v79, v14
	v_fma_f32 v249, 2.0, v244, v247
	v_fma_f32 v255, 2.0, v250, v253
	v_add_f32_e32 v247, v245, v247
	v_add_f32_e32 v253, v251, v253
	v_fma_f32 v246, -2.0, v244, v246
	v_fma_f32 v252, -2.0, v250, v252
	v_sub_f32_e32 v248, v248, v245
	v_sub_f32_e32 v254, v254, v251
	v_mul_f32_e32 v247, v247, v248
	v_mul_f32_e32 v253, v253, v254
	v_rcp_f32_e32 v247, v247
	v_rcp_f32_e32 v253, v253
	v_mul_f32_e32 v249, v249, v246
	v_mul_f32_e32 v255, v255, v252
	v_mul_f32_e32 v249, v249, v247
	v_mul_f32_e32 v255, v255, v253
	v_add_f32_e32 v20, v20, v249
	v_add_f32_e32 v20, v20, v255
	v_mul_f32_e32 v244, v84, v88
	v_mul_f32_e32 v250, v85, v89
	v_mul_f32_e32 v245, v88, v88
	v_mul_f32_e32 v251, v89, v89
	v_add_f32_e32 v246, v84, v88
	v_add_f32_e32 v252, v85, v89
	v_fma_f32 v245, v84, v84, v245
	v_fma_f32 v251, v85, v85, v251
	v_fma_f32 v247, v10, v246, v11
	v_fma_f32 v253, v10, v252, v11
	v_fma_f32 v246, v13, v96, v14
	v_fma_f32 v252, v13, v97, v14
	v_fma_f32 v248, v12, v92, v14
	v_fma_f32 v254, v12, v93, v14
	v_fma_f32 v249, 2.0, v244, v247
	v_fma_f32 v255, 2.0, v250, v253
	v_add_f32_e32 v247, v245, v247
	v_add_f32_e32 v253, v251, v253
	v_fma_f32 v246, -2.0, v244, v246
	v_fma_f32 v252, -2.0, v250, v252
	v_sub_f32_e32 v248, v248, v245
	v_sub_f32_e32 v254, v254, v251
	v_mul_f32_e32 v247, v247, v248
	v_mul_f32_e32 v253, v253, v254
	v_rcp_f32_e32 v247, v247
	v_rcp_f32_e32 v253, v253
	v_mul_f32_e32 v249, v249, v246
	v_mul_f32_e32 v255, v255, v252
	v_mul_f32_e32 v249, v249, v247
	v_mul_f32_e32 v255, v255, v253
	v_fma_f32 v19, v249, v15, v19
	v_fma_f32 v19, v255, v16, v19
	v_mul_f32_e32 v244, v86, v90
	v_mul_f32_e32 v250, v87, v91
	v_mul_f32_e32 v245, v90, v90
	v_mul_f32_e32 v251, v91, v91
	v_add_f32_e32 v246, v86, v90
	v_add_f32_e32 v252, v87, v91
	v_fma_f32 v245, v86, v86, v245
	v_fma_f32 v251, v87, v87, v251
	v_fma_f32 v247, v10, v246, v11
	v_fma_f32 v253, v10, v252, v11
	v_fma_f32 v246, v13, v98, v14
	v_fma_f32 v252, v13, v99, v14
	v_fma_f32 v248, v12, v94, v14
	v_fma_f32 v254, v12, v95, v14
	v_fma_f32 v249, 2.0, v244, v247
	v_fma_f32 v255, 2.0, v250, v253
	v_add_f32_e32 v247, v245, v247
	v_add_f32_e32 v253, v251, v253
	v_fma_f32 v246, -2.0, v244, v246
	v_fma_f32 v252, -2.0, v250, v252
	v_sub_f32_e32 v248, v248, v245
	v_sub_f32_e32 v254, v254, v251
	v_mul_f32_e32 v247, v247, v248
	v_mul_f32_e32 v253, v253, v254
	v_rcp_f32_e32 v247, v247
	v_rcp_f32_e32 v253, v253
	v_mul_f32_e32 v249, v249, v246
	v_mul_f32_e32 v255, v255, v252
	v_mul_f32_e32 v249, v249, v247
	v_mul_f32_e32 v255, v255, v253
	v_fma_f32 v20, v249, v17, v20
	v_fma_f32 v20, v255, v18, v20
	s_waitcnt vmcnt(12)
	v_cvt_pk_f16_f32 v36, v100, v104
	v_cvt_pk_f16_f32 v52, v132, v136
	v_pk_add_f16 v36, v36, -0.5 op_sel_hi:[1,0]
	v_pk_add_f16 v52, v52, -0.5 op_sel_hi:[1,0]
	v_pk_mul_f16 v68, v52, v52
	v_pk_mul_f16 v84, v36, v52
	v_pk_fma_f16 v68, v36, v36, v68
	v_cvt_pk_f16_f32 v40, v101, v105
	v_cvt_pk_f16_f32 v56, v133, v137
	v_pk_add_f16 v40, v40, -0.5 op_sel_hi:[1,0]
	v_pk_add_f16 v56, v56, -0.5 op_sel_hi:[1,0]
	v_pk_mul_f16 v72, v56, v56
	v_pk_mul_f16 v88, v40, v56
	v_pk_fma_f16 v72, v40, v40, v72
	v_cvt_pk_f16_f32 v44, v102, v106
	v_cvt_pk_f16_f32 v60, v134, v138
	v_pk_add_f16 v44, v44, -0.5 op_sel_hi:[1,0]
	v_pk_add_f16 v60, v60, -0.5 op_sel_hi:[1,0]
	v_pk_mul_f16 v76, v60, v60
	v_pk_mul_f16 v92, v44, v60
	v_pk_fma_f16 v76, v44, v44, v76
	v_cvt_pk_f16_f32 v48, v103, v107
	v_cvt_pk_f16_f32 v64, v135, v139
	v_pk_add_f16 v48, v48, -0.5 op_sel_hi:[1,0]
	v_pk_add_f16 v64, v64, -0.5 op_sel_hi:[1,0]
	v_pk_mul_f16 v80, v64, v64
	v_pk_mul_f16 v96, v48, v64
	v_pk_fma_f16 v80, v48, v48, v80
	s_waitcnt vmcnt(8)
	v_cvt_pk_f16_f32 v37, v108, v112
	v_cvt_pk_f16_f32 v53, v140, v144
	v_pk_add_f16 v37, v37, -0.5 op_sel_hi:[1,0]
	v_pk_add_f16 v53, v53, -0.5 op_sel_hi:[1,0]
	v_pk_mul_f16 v69, v53, v53
	v_pk_mul_f16 v85, v37, v53
	v_pk_fma_f16 v69, v37, v37, v69
	v_cvt_pk_f16_f32 v41, v109, v113
	v_cvt_pk_f16_f32 v57, v141, v145
	v_pk_add_f16 v41, v41, -0.5 op_sel_hi:[1,0]
	v_pk_add_f16 v57, v57, -0.5 op_sel_hi:[1,0]
	v_pk_mul_f16 v73, v57, v57
	v_pk_mul_f16 v89, v41, v57
	v_pk_fma_f16 v73, v41, v41, v73
	v_cvt_pk_f16_f32 v45, v110, v114
	v_cvt_pk_f16_f32 v61, v142, v146
	v_pk_add_f16 v45, v45, -0.5 op_sel_hi:[1,0]
	v_pk_add_f16 v61, v61, -0.5 op_sel_hi:[1,0]
	v_pk_mul_f16 v77, v61, v61
	v_pk_mul_f16 v93, v45, v61
	v_pk_fma_f16 v77, v45, v45, v77
	v_cvt_pk_f16_f32 v49, v111, v115
	v_cvt_pk_f16_f32 v65, v143, v147
	v_pk_add_f16 v49, v49, -0.5 op_sel_hi:[1,0]
	v_pk_add_f16 v65, v65, -0.5 op_sel_hi:[1,0]
	v_pk_mul_f16 v81, v65, v65
	v_pk_mul_f16 v97, v49, v65
	v_pk_fma_f16 v81, v49, v49, v81
	s_waitcnt vmcnt(4)
	v_cvt_pk_f16_f32 v38, v116, v120
	v_cvt_pk_f16_f32 v54, v148, v152
	v_pk_add_f16 v38, v38, -0.5 op_sel_hi:[1,0]
	v_pk_add_f16 v54, v54, -0.5 op_sel_hi:[1,0]
	v_pk_mul_f16 v70, v54, v54
	v_pk_mul_f16 v86, v38, v54
	v_pk_fma_f16 v70, v38, v38, v70
	v_cvt_pk_f16_f32 v42, v117, v121
	v_cvt_pk_f16_f32 v58, v149, v153
	v_pk_add_f16 v42, v42, -0.5 op_sel_hi:[1,0]
	v_pk_add_f16 v58, v58, -0.5 op_sel_hi:[1,0]
	v_pk_mul_f16 v74, v58, v58
	v_pk_mul_f16 v90, v42, v58
	v_pk_fma_f16 v74, v42, v42, v74
	v_cvt_pk_f16_f32 v46, v118, v122
	v_cvt_pk_f16_f32 v62, v150, v154
	v_pk_add_f16 v46, v46, -0.5 op_sel_hi:[1,0]
	v_pk_add_f16 v62, v62, -0.5 op_sel_hi:[1,0]
	v_pk_mul_f16 v78, v62, v62
	v_pk_mul_f16 v94, v46, v62
	v_pk_fma_f16 v78, v46, v46, v78
	v_cvt_pk_f16_f32 v50, v119, v123
	v_cvt_pk_f16_f32 v66, v151, v155
	v_pk_add_f16 v50, v50, -0.5 op_sel_hi:[1,0]
	v_pk_add_f16 v66, v66, -0.5 op_sel_hi:[1,0]
	v_pk_mul_f16 v82, v66, v66
	v_pk_mul_f16 v98, v50, v66
	v_pk_fma_f16 v82, v50, v50, v82
	s_waitcnt vmcnt(0)
	v_cvt_pk_f16_f32 v39, v124, v128
	v_cvt_pk_f16_f32 v55, v156, v160
	v_pk_add_f16 v39, v39, -0.5 op_sel_hi:[1,0]
	v_pk_add_f16 v55, v55, -0.5 op_sel_hi:[1,0]
	v_pk_mul_f16 v71, v55, v55
	v_pk_mul_f16 v87, v39, v55
	v_pk_fma_f16 v71, v39, v39, v71
	v_cvt_pk_f16_f32 v43, v125, v129
	v_cvt_pk_f16_f32 v59, v157, v161
	v_pk_add_f16 v43, v43, -0.5 op_sel_hi:[1,0]
	v_pk_add_f16 v59, v59, -0.5 op_sel_hi:[1,0]
	v_pk_mul_f16 v75, v59, v59
	v_pk_mul_f16 v91, v43, v59
	v_pk_fma_f16 v75, v43, v43, v75
	v_cvt_pk_f16_f32 v47, v126, v130
	v_cvt_pk_f16_f32 v63, v158, v162
	v_pk_add_f16 v47, v47, -0.5 op_sel_hi:[1,0]
	v_pk_add_f16 v63, v63, -0.5 op_sel_hi:[1,0]
	v_pk_mul_f16 v79, v63, v63
	v_pk_mul_f16 v95, v47, v63
	v_pk_fma_f16 v79, v47, v47, v79
	v_cvt_pk_f16_f32 v51, v127, v131
	v_cvt_pk_f16_f32 v67, v159, v163
	v_pk_add_f16 v51, v51, -0.5 op_sel_hi:[1,0]
	v_pk_add_f16 v67, v67, -0.5 op_sel_hi:[1,0]
	v_pk_mul_f16 v83, v67, v67
	v_pk_mul_f16 v99, v51, v67
	v_pk_fma_f16 v83, v51, v51, v83
	v_mfma_f32_16x16x32_f16 v[132:135], v[164:167], v[28:31], 0
	v_mfma_f32_16x16x32_f16 v[136:139], v[168:171], v[28:31], 0
	v_mfma_f32_16x16x32_f16 v[140:143], v[172:175], v[28:31], 0
	v_mfma_f32_16x16x32_f16 v[144:147], v[176:179], v[28:31], 0
	v_mfma_f32_16x16x32_f16 v[132:135], v[36:39], v[32:35], v[132:135]
	v_mfma_f32_16x16x32_f16 v[136:139], v[40:43], v[32:35], v[136:139]
	v_mfma_f32_16x16x32_f16 v[140:143], v[44:47], v[32:35], v[140:143]
	v_mfma_f32_16x16x32_f16 v[144:147], v[48:51], v[32:35], v[144:147]
	v_mfma_f32_16x16x32_f16 v[148:151], v[180:183], v[28:31], 0
	v_mfma_f32_16x16x32_f16 v[152:155], v[184:187], v[28:31], 0
	v_mfma_f32_16x16x32_f16 v[156:159], v[188:191], v[28:31], 0
	v_mfma_f32_16x16x32_f16 v[160:163], v[192:195], v[28:31], 0
	v_mfma_f32_16x16x32_f16 v[148:151], v[52:55], v[32:35], v[148:151]
	v_mfma_f32_16x16x32_f16 v[152:155], v[56:59], v[32:35], v[152:155]
	v_mfma_f32_16x16x32_f16 v[156:159], v[60:63], v[32:35], v[156:159]
	v_mfma_f32_16x16x32_f16 v[160:163], v[64:67], v[32:35], v[160:163]
	v_cvt_pk_f16_f32 v100, v132, v136
	v_cvt_pk_f16_f32 v101, v140, v144
	v_cvt_pk_f16_f32 v102, v133, v137
	v_cvt_pk_f16_f32 v103, v141, v145
	v_cvt_pk_f16_f32 v104, v134, v138
	v_cvt_pk_f16_f32 v105, v142, v146
	v_cvt_pk_f16_f32 v106, v135, v139
	v_cvt_pk_f16_f32 v107, v143, v147
	v_mfma_f32_16x16x32_f16 v[132:135], v[196:199], v[28:31], 0
	v_mfma_f32_16x16x32_f16 v[136:139], v[200:203], v[28:31], 0
	v_mfma_f32_16x16x32_f16 v[140:143], v[204:207], v[28:31], 0
	v_mfma_f32_16x16x32_f16 v[144:147], v[208:211], v[28:31], 0
	v_mfma_f32_16x16x32_f16 v[132:135], v[68:71], v[32:35], v[132:135]
	v_mfma_f32_16x16x32_f16 v[136:139], v[72:75], v[32:35], v[136:139]
	v_mfma_f32_16x16x32_f16 v[140:143], v[76:79], v[32:35], v[140:143]
	v_mfma_f32_16x16x32_f16 v[144:147], v[80:83], v[32:35], v[144:147]
	v_cvt_pk_f16_f32 v108, v148, v152
	v_cvt_pk_f16_f32 v109, v156, v160
	v_cvt_pk_f16_f32 v110, v149, v153
	v_cvt_pk_f16_f32 v111, v157, v161
	v_cvt_pk_f16_f32 v112, v150, v154
	v_cvt_pk_f16_f32 v113, v158, v162
	v_cvt_pk_f16_f32 v114, v151, v155
	v_cvt_pk_f16_f32 v115, v159, v163
	v_mfma_f32_16x16x32_f16 v[148:151], v[212:215], v[28:31], 0
	v_mfma_f32_16x16x32_f16 v[152:155], v[216:219], v[28:31], 0
	v_mfma_f32_16x16x32_f16 v[156:159], v[220:223], v[28:31], 0
	v_mfma_f32_16x16x32_f16 v[160:163], v[224:227], v[28:31], 0
	v_mfma_f32_16x16x32_f16 v[148:151], v[84:87], v[32:35], v[148:151]
	v_mfma_f32_16x16x32_f16 v[152:155], v[88:91], v[32:35], v[152:155]
	v_mfma_f32_16x16x32_f16 v[156:159], v[92:95], v[32:35], v[156:159]
	v_mfma_f32_16x16x32_f16 v[160:163], v[96:99], v[32:35], v[160:163]
	v_cvt_pk_f16_f32 v116, v132, v136
	v_cvt_pk_f16_f32 v117, v140, v144
	v_cvt_pk_f16_f32 v118, v133, v137
	v_cvt_pk_f16_f32 v119, v141, v145
	v_cvt_pk_f16_f32 v120, v134, v138
	v_cvt_pk_f16_f32 v121, v142, v146
	v_cvt_pk_f16_f32 v122, v135, v139
	v_cvt_pk_f16_f32 v123, v143, v147
	v_cvt_pk_f16_f32 v124, v148, v152
	v_cvt_pk_f16_f32 v125, v156, v160
	v_cvt_pk_f16_f32 v126, v149, v153
	v_cvt_pk_f16_f32 v127, v157, v161
	v_cvt_pk_f16_f32 v128, v150, v154
	v_cvt_pk_f16_f32 v129, v158, v162
	v_cvt_pk_f16_f32 v130, v151, v155
	v_cvt_pk_f16_f32 v131, v159, v163
	global_load_dwordx4 v[164:167], v3, s[84:85] offset:0 nt
	global_load_dwordx4 v[168:171], v3, s[84:85] offset:2048 nt
	global_load_dwordx4 v[180:183], v3, s[88:89] offset:0 nt
	global_load_dwordx4 v[184:187], v3, s[88:89] offset:2048 nt
	global_load_dwordx4 v[172:175], v3, s[86:87] offset:0 nt
	global_load_dwordx4 v[176:179], v3, s[86:87] offset:2048 nt
	global_load_dwordx4 v[188:191], v3, s[90:91] offset:0 nt
	global_load_dwordx4 v[192:195], v3, s[90:91] offset:2048 nt
	s_mov_b64 exec, s[38:39]
	ds_write_b128 v4, v[104:107] offset:16384
	ds_write_b128 v4, v[112:115] offset:16896
	ds_write_b128 v4, v[120:123] offset:17408
	ds_write_b128 v4, v[128:131] offset:17920
	s_mov_b64 exec, -1
	s_waitcnt lgkmcnt(0)
	ds_write_b32 v6, v8 offset:32
	v_mfma_f32_16x16x32_f16 v[132:135], v[24:27], v[100:103], 0
	v_mfma_f32_16x16x32_f16 v[136:139], v[24:27], v[108:111], 0
	v_mfma_f32_16x16x32_f16 v[140:143], v[24:27], v[116:119], 0
	v_mfma_f32_16x16x32_f16 v[144:147], v[24:27], v[124:127], 0
	v_mfma_f32_16x16x32_f16 v[148:151], v[28:31], v[100:103], 0
	v_mfma_f32_16x16x32_f16 v[152:155], v[28:31], v[108:111], 0
	v_mfma_f32_16x16x32_f16 v[156:159], v[28:31], v[116:119], 0
	v_mfma_f32_16x16x32_f16 v[160:163], v[28:31], v[124:127], 0
	v_mfma_f32_16x16x32_f16 v[148:151], v[32:35], v[104:107], v[148:151]
	v_mfma_f32_16x16x32_f16 v[152:155], v[32:35], v[112:115], v[152:155]
	v_mfma_f32_16x16x32_f16 v[156:159], v[32:35], v[120:123], v[156:159]
	v_mfma_f32_16x16x32_f16 v[160:163], v[32:35], v[128:131], v[160:163]
	v_mul_f32_e32 v244, v132, v136
	v_mul_f32_e32 v250, v133, v137
	v_mul_f32_e32 v245, v136, v136
	v_mul_f32_e32 v251, v137, v137
	v_add_f32_e32 v246, v132, v136
	v_add_f32_e32 v252, v133, v137
	v_fma_f32 v245, v132, v132, v245
	v_fma_f32 v251, v133, v133, v251
	v_fma_f32 v247, v10, v246, v11
	v_fma_f32 v253, v10, v252, v11
	v_fma_f32 v246, v13, v144, v14
	v_fma_f32 v252, v13, v145, v14
	v_fma_f32 v248, v12, v140, v14
	v_fma_f32 v254, v12, v141, v14
	v_fma_f32 v249, 2.0, v244, v247
	v_fma_f32 v255, 2.0, v250, v253
	v_add_f32_e32 v247, v245, v247
	v_add_f32_e32 v253, v251, v253
	v_fma_f32 v246, -2.0, v244, v246
	v_fma_f32 v252, -2.0, v250, v252
	v_sub_f32_e32 v248, v248, v245
	v_sub_f32_e32 v254, v254, v251
	v_mul_f32_e32 v247, v247, v248
	v_mul_f32_e32 v253, v253, v254
	v_rcp_f32_e32 v247, v247
	v_rcp_f32_e32 v253, v253
	v_mul_f32_e32 v249, v249, v246
	v_mul_f32_e32 v255, v255, v252
	v_mul_f32_e32 v249, v249, v247
	v_mul_f32_e32 v255, v255, v253
	v_add_f32_e32 v19, v19, v249
	v_add_f32_e32 v19, v19, v255
	v_mul_f32_e32 v244, v134, v138
	v_mul_f32_e32 v250, v135, v139
	v_mul_f32_e32 v245, v138, v138
	v_mul_f32_e32 v251, v139, v139
	v_add_f32_e32 v246, v134, v138
	v_add_f32_e32 v252, v135, v139
	v_fma_f32 v245, v134, v134, v245
	v_fma_f32 v251, v135, v135, v251
	v_fma_f32 v247, v10, v246, v11
	v_fma_f32 v253, v10, v252, v11
	v_fma_f32 v246, v13, v146, v14
	v_fma_f32 v252, v13, v147, v14
	v_fma_f32 v248, v12, v142, v14
	v_fma_f32 v254, v12, v143, v14
	v_fma_f32 v249, 2.0, v244, v247
	v_fma_f32 v255, 2.0, v250, v253
	v_add_f32_e32 v247, v245, v247
	v_add_f32_e32 v253, v251, v253
	v_fma_f32 v246, -2.0, v244, v246
	v_fma_f32 v252, -2.0, v250, v252
	v_sub_f32_e32 v248, v248, v245
	v_sub_f32_e32 v254, v254, v251
	v_mul_f32_e32 v247, v247, v248
	v_mul_f32_e32 v253, v253, v254
	v_rcp_f32_e32 v247, v247
	v_rcp_f32_e32 v253, v253
	v_mul_f32_e32 v249, v249, v246
	v_mul_f32_e32 v255, v255, v252
	v_mul_f32_e32 v249, v249, v247
	v_mul_f32_e32 v255, v255, v253
	v_add_f32_e32 v20, v20, v249
	v_add_f32_e32 v20, v20, v255
	v_mfma_f32_16x16x32_f16 v[132:135], v[24:27], v[104:107], 0
	v_mfma_f32_16x16x32_f16 v[136:139], v[24:27], v[112:115], 0
	v_mfma_f32_16x16x32_f16 v[140:143], v[24:27], v[120:123], 0
	v_mfma_f32_16x16x32_f16 v[144:147], v[24:27], v[128:131], 0
	ds_read_b32 v23, v7 offset:32
	s_waitcnt lgkmcnt(0)
	v_cmp_ne_u32_e32 vcc, 0, v23
	s_cbranch_vccnz .Lq_go_1
.Lq_spin_1:
	s_sleep 1
	ds_read_b32 v23, v7 offset:32
	s_waitcnt lgkmcnt(0)
	v_cmp_eq_u32_e32 vcc, 0, v23
	s_cbranch_vccnz .Lq_spin_1
.Lq_go_1:
	ds_read_b128 v[228:231], v5 offset:16384
	ds_read_b128 v[232:235], v5 offset:16896
	ds_read_b128 v[236:239], v5 offset:17408
	ds_read_b128 v[240:243], v5 offset:17920
	v_mul_f32_e32 v244, v148, v152
	v_mul_f32_e32 v250, v149, v153
	v_mul_f32_e32 v245, v152, v152
	v_mul_f32_e32 v251, v153, v153
	v_add_f32_e32 v246, v148, v152
	v_add_f32_e32 v252, v149, v153
	v_fma_f32 v245, v148, v148, v245
	v_fma_f32 v251, v149, v149, v251
	v_fma_f32 v247, v10, v246, v11
	v_fma_f32 v253, v10, v252, v11
	v_fma_f32 v246, v13, v160, v14
	v_fma_f32 v252, v13, v161, v14
	v_fma_f32 v248, v12, v156, v14
	v_fma_f32 v254, v12, v157, v14
	v_fma_f32 v249, 2.0, v244, v247
	v_fma_f32 v255, 2.0, v250, v253
	v_add_f32_e32 v247, v245, v247
	v_add_f32_e32 v253, v251, v253
	v_fma_f32 v246, -2.0, v244, v246
	v_fma_f32 v252, -2.0, v250, v252
	v_sub_f32_e32 v248, v248, v245
	v_sub_f32_e32 v254, v254, v251
	v_mul_f32_e32 v247, v247, v248
	v_mul_f32_e32 v253, v253, v254
	v_rcp_f32_e32 v247, v247
	v_rcp_f32_e32 v253, v253
	v_mul_f32_e32 v249, v249, v246
	v_mul_f32_e32 v255, v255, v252
	v_mul_f32_e32 v249, v249, v247
	v_mul_f32_e32 v255, v255, v253
	v_add_f32_e32 v19, v19, v249
	v_add_f32_e32 v19, v19, v255
	v_mul_f32_e32 v244, v150, v154
	v_mul_f32_e32 v250, v151, v155
	v_mul_f32_e32 v245, v154, v154
	v_mul_f32_e32 v251, v155, v155
	v_add_f32_e32 v246, v150, v154
	v_add_f32_e32 v252, v151, v155
	v_fma_f32 v245, v150, v150, v245
	v_fma_f32 v251, v151, v151, v251
	v_fma_f32 v247, v10, v246, v11
	v_fma_f32 v253, v10, v252, v11
	v_fma_f32 v246, v13, v162, v14
	v_fma_f32 v252, v13, v163, v14
	v_fma_f32 v248, v12, v158, v14
	v_fma_f32 v254, v12, v159, v14
	v_fma_f32 v249, 2.0, v244, v247
	v_fma_f32 v255, 2.0, v250, v253
	v_add_f32_e32 v247, v245, v247
	v_add_f32_e32 v253, v251, v253
	v_fma_f32 v246, -2.0, v244, v246
	v_fma_f32 v252, -2.0, v250, v252
	v_sub_f32_e32 v248, v248, v245
	v_sub_f32_e32 v254, v254, v251
	v_mul_f32_e32 v247, v247, v248
	v_mul_f32_e32 v253, v253, v254
	v_rcp_f32_e32 v247, v247
	v_rcp_f32_e32 v253, v253
	v_mul_f32_e32 v249, v249, v246
	v_mul_f32_e32 v255, v255, v252
	v_mul_f32_e32 v249, v249, v247
	v_mul_f32_e32 v255, v255, v253
	v_add_f32_e32 v20, v20, v249
	v_add_f32_e32 v20, v20, v255
	s_waitcnt lgkmcnt(0)
	v_mfma_f32_16x16x32_f16 v[148:151], v[28:31], v[228:231], 0
	v_mfma_f32_16x16x32_f16 v[152:155], v[28:31], v[232:235], 0
	v_mfma_f32_16x16x32_f16 v[156:159], v[28:31], v[236:239], 0
	v_mfma_f32_16x16x32_f16 v[160:163], v[28:31], v[240:243], 0
	v_mfma_f32_16x16x32_f16 v[148:151], v[32:35], v[100:103], v[148:151]
	v_mfma_f32_16x16x32_f16 v[152:155], v[32:35], v[108:111], v[152:155]
	v_mfma_f32_16x16x32_f16 v[156:159], v[32:35], v[116:119], v[156:159]
	v_mfma_f32_16x16x32_f16 v[160:163], v[32:35], v[124:127], v[160:163]
	v_mul_f32_e32 v244, v132, v136
	v_mul_f32_e32 v250, v133, v137
	v_mul_f32_e32 v245, v136, v136
	v_mul_f32_e32 v251, v137, v137
	v_add_f32_e32 v246, v132, v136
	v_add_f32_e32 v252, v133, v137
	v_fma_f32 v245, v132, v132, v245
	v_fma_f32 v251, v133, v133, v251
	v_fma_f32 v247, v10, v246, v11
	v_fma_f32 v253, v10, v252, v11
	v_fma_f32 v246, v13, v144, v14
	v_fma_f32 v252, v13, v145, v14
	v_fma_f32 v248, v12, v140, v14
	v_fma_f32 v254, v12, v141, v14
	v_fma_f32 v249, 2.0, v244, v247
	v_fma_f32 v255, 2.0, v250, v253
	v_add_f32_e32 v247, v245, v247
	v_add_f32_e32 v253, v251, v253
	v_fma_f32 v246, -2.0, v244, v246
	v_fma_f32 v252, -2.0, v250, v252
	v_sub_f32_e32 v248, v248, v245
	v_sub_f32_e32 v254, v254, v251
	v_mul_f32_e32 v247, v247, v248
	v_mul_f32_e32 v253, v253, v254
	v_rcp_f32_e32 v247, v247
	v_rcp_f32_e32 v253, v253
	v_mul_f32_e32 v249, v249, v246
	v_mul_f32_e32 v255, v255, v252
	v_mul_f32_e32 v249, v249, v247
	v_mul_f32_e32 v255, v255, v253
	v_add_f32_e32 v19, v19, v249
	v_add_f32_e32 v19, v19, v255
	v_mul_f32_e32 v244, v134, v138
	v_mul_f32_e32 v250, v135, v139
	v_mul_f32_e32 v245, v138, v138
	v_mul_f32_e32 v251, v139, v139
	v_add_f32_e32 v246, v134, v138
	v_add_f32_e32 v252, v135, v139
	v_fma_f32 v245, v134, v134, v245
	v_fma_f32 v251, v135, v135, v251
	v_fma_f32 v247, v10, v246, v11
	v_fma_f32 v253, v10, v252, v11
	v_fma_f32 v246, v13, v146, v14
	v_fma_f32 v252, v13, v147, v14
	v_fma_f32 v248, v12, v142, v14
	v_fma_f32 v254, v12, v143, v14
	v_fma_f32 v249, 2.0, v244, v247
	v_fma_f32 v255, 2.0, v250, v253
	v_add_f32_e32 v247, v245, v247
	v_add_f32_e32 v253, v251, v253
	v_fma_f32 v246, -2.0, v244, v246
	v_fma_f32 v252, -2.0, v250, v252
	v_sub_f32_e32 v248, v248, v245
	v_sub_f32_e32 v254, v254, v251
	v_mul_f32_e32 v247, v247, v248
	v_mul_f32_e32 v253, v253, v254
	v_rcp_f32_e32 v247, v247
	v_rcp_f32_e32 v253, v253
	v_mul_f32_e32 v249, v249, v246
	v_mul_f32_e32 v255, v255, v252
	v_mul_f32_e32 v249, v249, v247
	v_mul_f32_e32 v255, v255, v253
	v_add_f32_e32 v20, v20, v249
	v_add_f32_e32 v20, v20, v255
	v_mul_f32_e32 v244, v148, v152
	v_mul_f32_e32 v250, v149, v153
	v_mul_f32_e32 v245, v152, v152
	v_mul_f32_e32 v251, v153, v153
	v_add_f32_e32 v246, v148, v152
	v_add_f32_e32 v252, v149, v153
	v_fma_f32 v245, v148, v148, v245
	v_fma_f32 v251, v149, v149, v251
	v_fma_f32 v247, v10, v246, v11
	v_fma_f32 v253, v10, v252, v11
	v_fma_f32 v246, v13, v160, v14
	v_fma_f32 v252, v13, v161, v14
	v_fma_f32 v248, v12, v156, v14
	v_fma_f32 v254, v12, v157, v14
	v_fma_f32 v249, 2.0, v244, v247
	v_fma_f32 v255, 2.0, v250, v253
	v_add_f32_e32 v247, v245, v247
	v_add_f32_e32 v253, v251, v253
	v_fma_f32 v246, -2.0, v244, v246
	v_fma_f32 v252, -2.0, v250, v252
	v_sub_f32_e32 v248, v248, v245
	v_sub_f32_e32 v254, v254, v251
	v_mul_f32_e32 v247, v247, v248
	v_mul_f32_e32 v253, v253, v254
	v_rcp_f32_e32 v247, v247
	v_rcp_f32_e32 v253, v253
	v_mul_f32_e32 v249, v249, v246
	v_mul_f32_e32 v255, v255, v252
	v_mul_f32_e32 v249, v249, v247
	v_mul_f32_e32 v255, v255, v253
	v_fma_f32 v19, v249, v15, v19
	v_fma_f32 v19, v255, v16, v19
	v_mul_f32_e32 v244, v150, v154
	v_mul_f32_e32 v250, v151, v155
	v_mul_f32_e32 v245, v154, v154
	v_mul_f32_e32 v251, v155, v155
	v_add_f32_e32 v246, v150, v154
	v_add_f32_e32 v252, v151, v155
	v_fma_f32 v245, v150, v150, v245
	v_fma_f32 v251, v151, v151, v251
	v_fma_f32 v247, v10, v246, v11
	v_fma_f32 v253, v10, v252, v11
	v_fma_f32 v246, v13, v162, v14
	v_fma_f32 v252, v13, v163, v14
	v_fma_f32 v248, v12, v158, v14
	v_fma_f32 v254, v12, v159, v14
	v_fma_f32 v249, 2.0, v244, v247
	v_fma_f32 v255, 2.0, v250, v253
	v_add_f32_e32 v247, v245, v247
	v_add_f32_e32 v253, v251, v253
	v_fma_f32 v246, -2.0, v244, v246
	v_fma_f32 v252, -2.0, v250, v252
	v_sub_f32_e32 v248, v248, v245
	v_sub_f32_e32 v254, v254, v251
	v_mul_f32_e32 v247, v247, v248
	v_mul_f32_e32 v253, v253, v254
	v_rcp_f32_e32 v247, v247
	v_rcp_f32_e32 v253, v253
	v_mul_f32_e32 v249, v249, v246
	v_mul_f32_e32 v255, v255, v252
	v_mul_f32_e32 v249, v249, v247
	v_mul_f32_e32 v255, v255, v253
	v_fma_f32 v20, v249, v17, v20
	v_fma_f32 v20, v255, v18, v20
	v_mfma_f32_16x16x32_f16 v[132:135], v[36:39], v[24:27], 0
	v_mfma_f32_16x16x32_f16 v[136:139], v[40:43], v[24:27], 0
	v_mfma_f32_16x16x32_f16 v[140:143], v[44:47], v[24:27], 0
	v_mfma_f32_16x16x32_f16 v[144:147], v[48:51], v[24:27], 0
	v_mfma_f32_16x16x32_f16 v[148:151], v[52:55], v[24:27], 0
	v_mfma_f32_16x16x32_f16 v[152:155], v[56:59], v[24:27], 0
	v_mfma_f32_16x16x32_f16 v[156:159], v[60:63], v[24:27], 0
	v_mfma_f32_16x16x32_f16 v[160:163], v[64:67], v[24:27], 0
	s_nop 1
	v_cvt_pk_f16_f32 v100, v132, v136
	s_nop 0
	v_cvt_pk_f16_f32 v101, v140, v144
	v_cvt_pk_f16_f32 v102, v133, v137
	v_cvt_pk_f16_f32 v103, v141, v145
	v_cvt_pk_f16_f32 v104, v134, v138
	v_cvt_pk_f16_f32 v105, v142, v146
	v_cvt_pk_f16_f32 v106, v135, v139
	v_cvt_pk_f16_f32 v107, v143, v147
	v_mfma_f32_16x16x32_f16 v[132:135], v[68:71], v[24:27], 0
	v_mfma_f32_16x16x32_f16 v[136:139], v[72:75], v[24:27], 0
	v_mfma_f32_16x16x32_f16 v[140:143], v[76:79], v[24:27], 0
	v_mfma_f32_16x16x32_f16 v[144:147], v[80:83], v[24:27], 0
	v_cvt_pk_f16_f32 v108, v148, v152
	v_cvt_pk_f16_f32 v109, v156, v160
	v_cvt_pk_f16_f32 v110, v149, v153
	v_cvt_pk_f16_f32 v111, v157, v161
	v_cvt_pk_f16_f32 v112, v150, v154
	v_cvt_pk_f16_f32 v113, v158, v162
	v_cvt_pk_f16_f32 v114, v151, v155
	v_cvt_pk_f16_f32 v115, v159, v163
	v_mfma_f32_16x16x32_f16 v[148:151], v[84:87], v[24:27], 0
	v_mfma_f32_16x16x32_f16 v[152:155], v[88:91], v[24:27], 0
	v_mfma_f32_16x16x32_f16 v[156:159], v[92:95], v[24:27], 0
	v_mfma_f32_16x16x32_f16 v[160:163], v[96:99], v[24:27], 0
	v_cvt_pk_f16_f32 v116, v132, v136
	v_cvt_pk_f16_f32 v117, v140, v144
	v_cvt_pk_f16_f32 v118, v133, v137
	v_cvt_pk_f16_f32 v119, v141, v145
	v_cvt_pk_f16_f32 v120, v134, v138
	v_cvt_pk_f16_f32 v121, v142, v146
	v_cvt_pk_f16_f32 v122, v135, v139
	v_cvt_pk_f16_f32 v123, v143, v147
	v_cvt_pk_f16_f32 v124, v148, v152
	v_cvt_pk_f16_f32 v125, v156, v160
	v_cvt_pk_f16_f32 v126, v149, v153
	v_cvt_pk_f16_f32 v127, v157, v161
	v_cvt_pk_f16_f32 v128, v150, v154
	v_cvt_pk_f16_f32 v129, v158, v162
	v_cvt_pk_f16_f32 v130, v151, v155
	v_cvt_pk_f16_f32 v131, v159, v163
	s_mov_b64 exec, s[38:39]
	ds_write_b128 v4, v[104:107] offset:32768
	ds_write_b128 v4, v[112:115] offset:33280
	ds_write_b128 v4, v[120:123] offset:33792
	ds_write_b128 v4, v[128:131] offset:34304
	s_mov_b64 exec, -1
	s_waitcnt lgkmcnt(0)
	ds_write_b32 v6, v8 offset:64
	v_mfma_f32_16x16x32_f16 v[132:135], v[24:27], v[100:103], 0
	v_mfma_f32_16x16x32_f16 v[136:139], v[24:27], v[108:111], 0
	v_mfma_f32_16x16x32_f16 v[140:143], v[24:27], v[116:119], 0
	v_mfma_f32_16x16x32_f16 v[144:147], v[24:27], v[124:127], 0
	v_mfma_f32_16x16x32_f16 v[148:151], v[28:31], v[100:103], 0
	v_mfma_f32_16x16x32_f16 v[152:155], v[28:31], v[108:111], 0
	v_mfma_f32_16x16x32_f16 v[156:159], v[28:31], v[116:119], 0
	v_mfma_f32_16x16x32_f16 v[160:163], v[28:31], v[124:127], 0
	v_mfma_f32_16x16x32_f16 v[148:151], v[32:35], v[104:107], v[148:151]
	v_mfma_f32_16x16x32_f16 v[152:155], v[32:35], v[112:115], v[152:155]
	v_mfma_f32_16x16x32_f16 v[156:159], v[32:35], v[120:123], v[156:159]
	v_mfma_f32_16x16x32_f16 v[160:163], v[32:35], v[128:131], v[160:163]
	v_mul_f32_e32 v244, v132, v136
	v_mul_f32_e32 v250, v133, v137
	v_mul_f32_e32 v245, v136, v136
	v_mul_f32_e32 v251, v137, v137
	v_add_f32_e32 v246, v132, v136
	v_add_f32_e32 v252, v133, v137
	v_fma_f32 v245, v132, v132, v245
	v_fma_f32 v251, v133, v133, v251
	v_fma_f32 v247, v10, v246, v11
	v_fma_f32 v253, v10, v252, v11
	v_fma_f32 v246, v13, v144, v14
	v_fma_f32 v252, v13, v145, v14
	v_fma_f32 v248, v12, v140, v14
	v_fma_f32 v254, v12, v141, v14
	v_fma_f32 v249, 2.0, v244, v247
	v_fma_f32 v255, 2.0, v250, v253
	v_add_f32_e32 v247, v245, v247
	v_add_f32_e32 v253, v251, v253
	v_fma_f32 v246, -2.0, v244, v246
	v_fma_f32 v252, -2.0, v250, v252
	v_sub_f32_e32 v248, v248, v245
	v_sub_f32_e32 v254, v254, v251
	v_mul_f32_e32 v247, v247, v248
	v_mul_f32_e32 v253, v253, v254
	v_rcp_f32_e32 v247, v247
	v_rcp_f32_e32 v253, v253
	v_mul_f32_e32 v249, v249, v246
	v_mul_f32_e32 v255, v255, v252
	v_mul_f32_e32 v249, v249, v247
	v_mul_f32_e32 v255, v255, v253
	v_add_f32_e32 v19, v19, v249
	v_add_f32_e32 v19, v19, v255
	v_mul_f32_e32 v244, v134, v138
	v_mul_f32_e32 v250, v135, v139
	v_mul_f32_e32 v245, v138, v138
	v_mul_f32_e32 v251, v139, v139
	v_add_f32_e32 v246, v134, v138
	v_add_f32_e32 v252, v135, v139
	v_fma_f32 v245, v134, v134, v245
	v_fma_f32 v251, v135, v135, v251
	v_fma_f32 v247, v10, v246, v11
	v_fma_f32 v253, v10, v252, v11
	v_fma_f32 v246, v13, v146, v14
	v_fma_f32 v252, v13, v147, v14
	v_fma_f32 v248, v12, v142, v14
	v_fma_f32 v254, v12, v143, v14
	v_fma_f32 v249, 2.0, v244, v247
	v_fma_f32 v255, 2.0, v250, v253
	v_add_f32_e32 v247, v245, v247
	v_add_f32_e32 v253, v251, v253
	v_fma_f32 v246, -2.0, v244, v246
	v_fma_f32 v252, -2.0, v250, v252
	v_sub_f32_e32 v248, v248, v245
	v_sub_f32_e32 v254, v254, v251
	v_mul_f32_e32 v247, v247, v248
	v_mul_f32_e32 v253, v253, v254
	v_rcp_f32_e32 v247, v247
	v_rcp_f32_e32 v253, v253
	v_mul_f32_e32 v249, v249, v246
	v_mul_f32_e32 v255, v255, v252
	v_mul_f32_e32 v249, v249, v247
	v_mul_f32_e32 v255, v255, v253
	v_add_f32_e32 v20, v20, v249
	v_add_f32_e32 v20, v20, v255
	v_mfma_f32_16x16x32_f16 v[132:135], v[24:27], v[104:107], 0
	v_mfma_f32_16x16x32_f16 v[136:139], v[24:27], v[112:115], 0
	v_mfma_f32_16x16x32_f16 v[140:143], v[24:27], v[120:123], 0
	v_mfma_f32_16x16x32_f16 v[144:147], v[24:27], v[128:131], 0
	ds_read_b32 v23, v7 offset:64
	s_waitcnt lgkmcnt(0)
	v_cmp_ne_u32_e32 vcc, 0, v23
	s_cbranch_vccnz .Lq_go_2
.Lq_spin_2:
	s_sleep 1
	ds_read_b32 v23, v7 offset:64
	s_waitcnt lgkmcnt(0)
	v_cmp_eq_u32_e32 vcc, 0, v23
	s_cbranch_vccnz .Lq_spin_2
.Lq_go_2:
	ds_read_b128 v[228:231], v5 offset:32768
	ds_read_b128 v[232:235], v5 offset:33280
	ds_read_b128 v[236:239], v5 offset:33792
	ds_read_b128 v[240:243], v5 offset:34304
	v_mul_f32_e32 v244, v148, v152
	v_mul_f32_e32 v250, v149, v153
	v_mul_f32_e32 v245, v152, v152
	v_mul_f32_e32 v251, v153, v153
	v_add_f32_e32 v246, v148, v152
	v_add_f32_e32 v252, v149, v153
	v_fma_f32 v245, v148, v148, v245
	v_fma_f32 v251, v149, v149, v251
	v_fma_f32 v247, v10, v246, v11
	v_fma_f32 v253, v10, v252, v11
	v_fma_f32 v246, v13, v160, v14
	v_fma_f32 v252, v13, v161, v14
	v_fma_f32 v248, v12, v156, v14
	v_fma_f32 v254, v12, v157, v14
	v_fma_f32 v249, 2.0, v244, v247
	v_fma_f32 v255, 2.0, v250, v253
	v_add_f32_e32 v247, v245, v247
	v_add_f32_e32 v253, v251, v253
	v_fma_f32 v246, -2.0, v244, v246
	v_fma_f32 v252, -2.0, v250, v252
	v_sub_f32_e32 v248, v248, v245
	v_sub_f32_e32 v254, v254, v251
	v_mul_f32_e32 v247, v247, v248
	v_mul_f32_e32 v253, v253, v254
	v_rcp_f32_e32 v247, v247
	v_rcp_f32_e32 v253, v253
	v_mul_f32_e32 v249, v249, v246
	v_mul_f32_e32 v255, v255, v252
	v_mul_f32_e32 v249, v249, v247
	v_mul_f32_e32 v255, v255, v253
	v_add_f32_e32 v19, v19, v249
	v_add_f32_e32 v19, v19, v255
	v_mul_f32_e32 v244, v150, v154
	v_mul_f32_e32 v250, v151, v155
	v_mul_f32_e32 v245, v154, v154
	v_mul_f32_e32 v251, v155, v155
	v_add_f32_e32 v246, v150, v154
	v_add_f32_e32 v252, v151, v155
	v_fma_f32 v245, v150, v150, v245
	v_fma_f32 v251, v151, v151, v251
	v_fma_f32 v247, v10, v246, v11
	v_fma_f32 v253, v10, v252, v11
	v_fma_f32 v246, v13, v162, v14
	v_fma_f32 v252, v13, v163, v14
	v_fma_f32 v248, v12, v158, v14
	v_fma_f32 v254, v12, v159, v14
	v_fma_f32 v249, 2.0, v244, v247
	v_fma_f32 v255, 2.0, v250, v253
	v_add_f32_e32 v247, v245, v247
	v_add_f32_e32 v253, v251, v253
	v_fma_f32 v246, -2.0, v244, v246
	v_fma_f32 v252, -2.0, v250, v252
	v_sub_f32_e32 v248, v248, v245
	v_sub_f32_e32 v254, v254, v251
	v_mul_f32_e32 v247, v247, v248
	v_mul_f32_e32 v253, v253, v254
	v_rcp_f32_e32 v247, v247
	v_rcp_f32_e32 v253, v253
	v_mul_f32_e32 v249, v249, v246
	v_mul_f32_e32 v255, v255, v252
	v_mul_f32_e32 v249, v249, v247
	v_mul_f32_e32 v255, v255, v253
	v_add_f32_e32 v20, v20, v249
	v_add_f32_e32 v20, v20, v255
	s_waitcnt lgkmcnt(0)
	v_mfma_f32_16x16x32_f16 v[148:151], v[28:31], v[228:231], 0
	v_mfma_f32_16x16x32_f16 v[152:155], v[28:31], v[232:235], 0
	v_mfma_f32_16x16x32_f16 v[156:159], v[28:31], v[236:239], 0
	v_mfma_f32_16x16x32_f16 v[160:163], v[28:31], v[240:243], 0
	v_mfma_f32_16x16x32_f16 v[148:151], v[32:35], v[100:103], v[148:151]
	v_mfma_f32_16x16x32_f16 v[152:155], v[32:35], v[108:111], v[152:155]
	v_mfma_f32_16x16x32_f16 v[156:159], v[32:35], v[116:119], v[156:159]
	v_mfma_f32_16x16x32_f16 v[160:163], v[32:35], v[124:127], v[160:163]
	v_mul_f32_e32 v244, v132, v136
	v_mul_f32_e32 v250, v133, v137
	v_mul_f32_e32 v245, v136, v136
	v_mul_f32_e32 v251, v137, v137
	v_add_f32_e32 v246, v132, v136
	v_add_f32_e32 v252, v133, v137
	v_fma_f32 v245, v132, v132, v245
	v_fma_f32 v251, v133, v133, v251
	v_fma_f32 v247, v10, v246, v11
	v_fma_f32 v253, v10, v252, v11
	v_fma_f32 v246, v13, v144, v14
	v_fma_f32 v252, v13, v145, v14
	v_fma_f32 v248, v12, v140, v14
	v_fma_f32 v254, v12, v141, v14
	v_fma_f32 v249, 2.0, v244, v247
	v_fma_f32 v255, 2.0, v250, v253
	v_add_f32_e32 v247, v245, v247
	v_add_f32_e32 v253, v251, v253
	v_fma_f32 v246, -2.0, v244, v246
	v_fma_f32 v252, -2.0, v250, v252
	v_sub_f32_e32 v248, v248, v245
	v_sub_f32_e32 v254, v254, v251
	v_mul_f32_e32 v247, v247, v248
	v_mul_f32_e32 v253, v253, v254
	v_rcp_f32_e32 v247, v247
	v_rcp_f32_e32 v253, v253
	v_mul_f32_e32 v249, v249, v246
	v_mul_f32_e32 v255, v255, v252
	v_mul_f32_e32 v249, v249, v247
	v_mul_f32_e32 v255, v255, v253
	v_add_f32_e32 v19, v19, v249
	v_add_f32_e32 v19, v19, v255
	v_mul_f32_e32 v244, v134, v138
	v_mul_f32_e32 v250, v135, v139
	v_mul_f32_e32 v245, v138, v138
	v_mul_f32_e32 v251, v139, v139
	v_add_f32_e32 v246, v134, v138
	v_add_f32_e32 v252, v135, v139
	v_fma_f32 v245, v134, v134, v245
	v_fma_f32 v251, v135, v135, v251
	v_fma_f32 v247, v10, v246, v11
	v_fma_f32 v253, v10, v252, v11
	v_fma_f32 v246, v13, v146, v14
	v_fma_f32 v252, v13, v147, v14
	v_fma_f32 v248, v12, v142, v14
	v_fma_f32 v254, v12, v143, v14
	v_fma_f32 v249, 2.0, v244, v247
	v_fma_f32 v255, 2.0, v250, v253
	v_add_f32_e32 v247, v245, v247
	v_add_f32_e32 v253, v251, v253
	v_fma_f32 v246, -2.0, v244, v246
	v_fma_f32 v252, -2.0, v250, v252
	v_sub_f32_e32 v248, v248, v245
	v_sub_f32_e32 v254, v254, v251
	v_mul_f32_e32 v247, v247, v248
	v_mul_f32_e32 v253, v253, v254
	v_rcp_f32_e32 v247, v247
	v_rcp_f32_e32 v253, v253
	v_mul_f32_e32 v249, v249, v246
	v_mul_f32_e32 v255, v255, v252
	v_mul_f32_e32 v249, v249, v247
	v_mul_f32_e32 v255, v255, v253
	v_add_f32_e32 v20, v20, v249
	v_add_f32_e32 v20, v20, v255
	v_mul_f32_e32 v244, v148, v152
	v_mul_f32_e32 v250, v149, v153
	v_mul_f32_e32 v245, v152, v152
	v_mul_f32_e32 v251, v153, v153
	v_add_f32_e32 v246, v148, v152
	v_add_f32_e32 v252, v149, v153
	v_fma_f32 v245, v148, v148, v245
	v_fma_f32 v251, v149, v149, v251
	v_fma_f32 v247, v10, v246, v11
	v_fma_f32 v253, v10, v252, v11
	v_fma_f32 v246, v13, v160, v14
	v_fma_f32 v252, v13, v161, v14
	v_fma_f32 v248, v12, v156, v14
	v_fma_f32 v254, v12, v157, v14
	v_fma_f32 v249, 2.0, v244, v247
	v_fma_f32 v255, 2.0, v250, v253
	v_add_f32_e32 v247, v245, v247
	v_add_f32_e32 v253, v251, v253
	v_fma_f32 v246, -2.0, v244, v246
	v_fma_f32 v252, -2.0, v250, v252
	v_sub_f32_e32 v248, v248, v245
	v_sub_f32_e32 v254, v254, v251
	v_mul_f32_e32 v247, v247, v248
	v_mul_f32_e32 v253, v253, v254
	v_rcp_f32_e32 v247, v247
	v_rcp_f32_e32 v253, v253
	v_mul_f32_e32 v249, v249, v246
	v_mul_f32_e32 v255, v255, v252
	v_mul_f32_e32 v249, v249, v247
	v_mul_f32_e32 v255, v255, v253
	v_fma_f32 v19, v249, v15, v19
	v_fma_f32 v19, v255, v16, v19
	v_mul_f32_e32 v244, v150, v154
	v_mul_f32_e32 v250, v151, v155
	v_mul_f32_e32 v245, v154, v154
	v_mul_f32_e32 v251, v155, v155
	v_add_f32_e32 v246, v150, v154
	v_add_f32_e32 v252, v151, v155
	v_fma_f32 v245, v150, v150, v245
	v_fma_f32 v251, v151, v151, v251
	v_fma_f32 v247, v10, v246, v11
	v_fma_f32 v253, v10, v252, v11
	v_fma_f32 v246, v13, v162, v14
	v_fma_f32 v252, v13, v163, v14
	v_fma_f32 v248, v12, v158, v14
	v_fma_f32 v254, v12, v159, v14
	v_fma_f32 v249, 2.0, v244, v247
	v_fma_f32 v255, 2.0, v250, v253
	v_add_f32_e32 v247, v245, v247
	v_add_f32_e32 v253, v251, v253
	v_fma_f32 v246, -2.0, v244, v246
	v_fma_f32 v252, -2.0, v250, v252
	v_sub_f32_e32 v248, v248, v245
	v_sub_f32_e32 v254, v254, v251
	v_mul_f32_e32 v247, v247, v248
	v_mul_f32_e32 v253, v253, v254
	v_rcp_f32_e32 v247, v247
	v_rcp_f32_e32 v253, v253
	v_mul_f32_e32 v249, v249, v246
	v_mul_f32_e32 v255, v255, v252
	v_mul_f32_e32 v249, v249, v247
	v_mul_f32_e32 v255, v255, v253
	v_fma_f32 v20, v249, v17, v20
	v_fma_f32 v20, v255, v18, v20
	s_waitcnt vmcnt(4)
	v_cvt_pk_f16_f32 v100, v164, v168
	v_cvt_pk_f16_f32 v116, v180, v184
	v_pk_add_f16 v100, v100, -0.5 op_sel_hi:[1,0]
	v_pk_add_f16 v116, v116, -0.5 op_sel_hi:[1,0]
	v_pk_mul_f16 v132, v116, v116
	v_pk_mul_f16 v148, v100, v116
	v_pk_fma_f16 v132, v100, v100, v132
	v_cvt_pk_f16_f32 v104, v165, v169
	v_cvt_pk_f16_f32 v120, v181, v185
	v_pk_add_f16 v104, v104, -0.5 op_sel_hi:[1,0]
	v_pk_add_f16 v120, v120, -0.5 op_sel_hi:[1,0]
	v_pk_mul_f16 v136, v120, v120
	v_pk_mul_f16 v152, v104, v120
	v_pk_fma_f16 v136, v104, v104, v136
	v_cvt_pk_f16_f32 v108, v166, v170
	v_cvt_pk_f16_f32 v124, v182, v186
	v_pk_add_f16 v108, v108, -0.5 op_sel_hi:[1,0]
	v_pk_add_f16 v124, v124, -0.5 op_sel_hi:[1,0]
	v_pk_mul_f16 v140, v124, v124
	v_pk_mul_f16 v156, v108, v124
	v_pk_fma_f16 v140, v108, v108, v140
	v_cvt_pk_f16_f32 v112, v167, v171
	v_cvt_pk_f16_f32 v128, v183, v187
	v_pk_add_f16 v112, v112, -0.5 op_sel_hi:[1,0]
	v_pk_add_f16 v128, v128, -0.5 op_sel_hi:[1,0]
	v_pk_mul_f16 v144, v128, v128
	v_pk_mul_f16 v160, v112, v128
	v_pk_fma_f16 v144, v112, v112, v144
	s_waitcnt vmcnt(0)
	v_cvt_pk_f16_f32 v101, v172, v176
	v_cvt_pk_f16_f32 v117, v188, v192
	v_pk_add_f16 v101, v101, -0.5 op_sel_hi:[1,0]
	v_pk_add_f16 v117, v117, -0.5 op_sel_hi:[1,0]
	v_pk_mul_f16 v133, v117, v117
	v_pk_mul_f16 v149, v101, v117
	v_pk_fma_f16 v133, v101, v101, v133
	v_cvt_pk_f16_f32 v105, v173, v177
	v_cvt_pk_f16_f32 v121, v189, v193
	v_pk_add_f16 v105, v105, -0.5 op_sel_hi:[1,0]
	v_pk_add_f16 v121, v121, -0.5 op_sel_hi:[1,0]
	v_pk_mul_f16 v137, v121, v121
	v_pk_mul_f16 v153, v105, v121
	v_pk_fma_f16 v137, v105, v105, v137
	v_cvt_pk_f16_f32 v109, v174, v178
	v_cvt_pk_f16_f32 v125, v190, v194
	v_pk_add_f16 v109, v109, -0.5 op_sel_hi:[1,0]
	v_pk_add_f16 v125, v125, -0.5 op_sel_hi:[1,0]
	v_pk_mul_f16 v141, v125, v125
	v_pk_mul_f16 v157, v109, v125
	v_pk_fma_f16 v141, v109, v109, v141
	v_cvt_pk_f16_f32 v113, v175, v179
	v_cvt_pk_f16_f32 v129, v191, v195
	v_pk_add_f16 v113, v113, -0.5 op_sel_hi:[1,0]
	v_pk_add_f16 v129, v129, -0.5 op_sel_hi:[1,0]
	v_pk_mul_f16 v145, v129, v129
	v_pk_mul_f16 v161, v113, v129
	v_pk_fma_f16 v145, v113, v113, v145
	v_mov_b32_e32 v102, v100
	v_mov_b32_e32 v103, v101
	v_mov_b32_e32 v106, v104
	v_mov_b32_e32 v107, v105
	v_mov_b32_e32 v110, v108
	v_mov_b32_e32 v111, v109
	v_mov_b32_e32 v114, v112
	v_mov_b32_e32 v115, v113
	v_mov_b32_e32 v118, v116
	v_mov_b32_e32 v119, v117
	v_mov_b32_e32 v122, v120
	v_mov_b32_e32 v123, v121
	v_mov_b32_e32 v126, v124
	v_mov_b32_e32 v127, v125
	v_mov_b32_e32 v130, v128
	v_mov_b32_e32 v131, v129
	v_mov_b32_e32 v134, v132
	v_mov_b32_e32 v135, v133
	v_mov_b32_e32 v138, v136
	v_mov_b32_e32 v139, v137
	v_mov_b32_e32 v142, v140
	v_mov_b32_e32 v143, v141
	v_mov_b32_e32 v146, v144
	v_mov_b32_e32 v147, v145
	v_mov_b32_e32 v150, v148
	v_mov_b32_e32 v151, v149
	v_mov_b32_e32 v154, v152
	v_mov_b32_e32 v155, v153
	v_mov_b32_e32 v158, v156
	v_mov_b32_e32 v159, v157
	v_mov_b32_e32 v162, v160
	v_mov_b32_e32 v163, v161
	v_permlane32_swap_b32_e32 v100, v102
	v_permlane32_swap_b32_e32 v101, v103
	v_permlane32_swap_b32_e32 v104, v106
	v_permlane32_swap_b32_e32 v105, v107
	v_permlane32_swap_b32_e32 v108, v110
	v_permlane32_swap_b32_e32 v109, v111
	v_permlane32_swap_b32_e32 v112, v114
	v_permlane32_swap_b32_e32 v113, v115
	v_permlane32_swap_b32_e32 v116, v118
	v_permlane32_swap_b32_e32 v117, v119
	v_permlane32_swap_b32_e32 v120, v122
	v_permlane32_swap_b32_e32 v121, v123
	v_permlane32_swap_b32_e32 v124, v126
	v_permlane32_swap_b32_e32 v125, v127
	v_permlane32_swap_b32_e32 v128, v130
	v_permlane32_swap_b32_e32 v129, v131
	v_permlane32_swap_b32_e32 v132, v134
	v_permlane32_swap_b32_e32 v133, v135
	v_permlane32_swap_b32_e32 v136, v138
	v_permlane32_swap_b32_e32 v137, v139
	v_permlane32_swap_b32_e32 v140, v142
	v_permlane32_swap_b32_e32 v141, v143
	v_permlane32_swap_b32_e32 v144, v146
	v_permlane32_swap_b32_e32 v145, v147
	v_permlane32_swap_b32_e32 v148, v150
	v_permlane32_swap_b32_e32 v149, v151
	v_permlane32_swap_b32_e32 v152, v154
	v_permlane32_swap_b32_e32 v153, v155
	v_permlane32_swap_b32_e32 v156, v158
	v_permlane32_swap_b32_e32 v157, v159
	v_permlane32_swap_b32_e32 v160, v162
	v_permlane32_swap_b32_e32 v161, v163
	v_mfma_f32_16x16x32_f16 v[196:199], v[36:39], v[28:31], 0
	v_mfma_f32_16x16x32_f16 v[200:203], v[40:43], v[28:31], 0
	v_mfma_f32_16x16x32_f16 v[204:207], v[44:47], v[28:31], 0
	v_mfma_f32_16x16x32_f16 v[208:211], v[48:51], v[28:31], 0
	v_mfma_f32_16x16x32_f16 v[196:199], v[100:103], v[32:35], v[196:199]
	v_mfma_f32_16x16x32_f16 v[200:203], v[104:107], v[32:35], v[200:203]
	v_mfma_f32_16x16x32_f16 v[204:207], v[108:111], v[32:35], v[204:207]
	v_mfma_f32_16x16x32_f16 v[208:211], v[112:115], v[32:35], v[208:211]
	v_mfma_f32_16x16x32_f16 v[212:215], v[52:55], v[28:31], 0
	v_mfma_f32_16x16x32_f16 v[216:219], v[56:59], v[28:31], 0
	v_mfma_f32_16x16x32_f16 v[220:223], v[60:63], v[28:31], 0
	v_mfma_f32_16x16x32_f16 v[224:227], v[64:67], v[28:31], 0
	v_mfma_f32_16x16x32_f16 v[212:215], v[116:119], v[32:35], v[212:215]
	v_mfma_f32_16x16x32_f16 v[216:219], v[120:123], v[32:35], v[216:219]
	v_mfma_f32_16x16x32_f16 v[220:223], v[124:127], v[32:35], v[220:223]
	v_mfma_f32_16x16x32_f16 v[224:227], v[128:131], v[32:35], v[224:227]
	v_cvt_pk_f16_f32 v164, v196, v200
	v_cvt_pk_f16_f32 v165, v204, v208
	v_cvt_pk_f16_f32 v166, v197, v201
	v_cvt_pk_f16_f32 v167, v205, v209
	v_cvt_pk_f16_f32 v168, v198, v202
	v_cvt_pk_f16_f32 v169, v206, v210
	v_cvt_pk_f16_f32 v170, v199, v203
	v_cvt_pk_f16_f32 v171, v207, v211
	v_mfma_f32_16x16x32_f16 v[196:199], v[68:71], v[28:31], 0
	v_mfma_f32_16x16x32_f16 v[200:203], v[72:75], v[28:31], 0
	v_mfma_f32_16x16x32_f16 v[204:207], v[76:79], v[28:31], 0
	v_mfma_f32_16x16x32_f16 v[208:211], v[80:83], v[28:31], 0
	v_mfma_f32_16x16x32_f16 v[196:199], v[132:135], v[32:35], v[196:199]
	v_mfma_f32_16x16x32_f16 v[200:203], v[136:139], v[32:35], v[200:203]
	v_mfma_f32_16x16x32_f16 v[204:207], v[140:143], v[32:35], v[204:207]
	v_mfma_f32_16x16x32_f16 v[208:211], v[144:147], v[32:35], v[208:211]
	v_cvt_pk_f16_f32 v172, v212, v216
	v_cvt_pk_f16_f32 v173, v220, v224
	v_cvt_pk_f16_f32 v174, v213, v217
	v_cvt_pk_f16_f32 v175, v221, v225
	v_cvt_pk_f16_f32 v176, v214, v218
	v_cvt_pk_f16_f32 v177, v222, v226
	v_cvt_pk_f16_f32 v178, v215, v219
	v_cvt_pk_f16_f32 v179, v223, v227
	v_mfma_f32_16x16x32_f16 v[212:215], v[84:87], v[28:31], 0
	v_mfma_f32_16x16x32_f16 v[216:219], v[88:91], v[28:31], 0
	v_mfma_f32_16x16x32_f16 v[220:223], v[92:95], v[28:31], 0
	v_mfma_f32_16x16x32_f16 v[224:227], v[96:99], v[28:31], 0
	v_mfma_f32_16x16x32_f16 v[212:215], v[148:151], v[32:35], v[212:215]
	v_mfma_f32_16x16x32_f16 v[216:219], v[152:155], v[32:35], v[216:219]
	v_mfma_f32_16x16x32_f16 v[220:223], v[156:159], v[32:35], v[220:223]
	v_mfma_f32_16x16x32_f16 v[224:227], v[160:163], v[32:35], v[224:227]
	v_cvt_pk_f16_f32 v180, v196, v200
	v_cvt_pk_f16_f32 v181, v204, v208
	v_cvt_pk_f16_f32 v182, v197, v201
	v_cvt_pk_f16_f32 v183, v205, v209
	v_cvt_pk_f16_f32 v184, v198, v202
	v_cvt_pk_f16_f32 v185, v206, v210
	v_cvt_pk_f16_f32 v186, v199, v203
	v_cvt_pk_f16_f32 v187, v207, v211
	v_cvt_pk_f16_f32 v188, v212, v216
	v_cvt_pk_f16_f32 v189, v220, v224
	v_cvt_pk_f16_f32 v190, v213, v217
	v_cvt_pk_f16_f32 v191, v221, v225
	v_cvt_pk_f16_f32 v192, v214, v218
	v_cvt_pk_f16_f32 v193, v222, v226
	v_cvt_pk_f16_f32 v194, v215, v219
	v_cvt_pk_f16_f32 v195, v223, v227
	s_mov_b64 exec, s[38:39]
	ds_write_b128 v4, v[168:171] offset:49152
	ds_write_b128 v4, v[176:179] offset:49664
	ds_write_b128 v4, v[184:187] offset:50176
	ds_write_b128 v4, v[192:195] offset:50688
	s_mov_b64 exec, -1
	s_waitcnt lgkmcnt(0)
	ds_write_b32 v6, v8 offset:96
	v_mfma_f32_16x16x32_f16 v[196:199], v[24:27], v[164:167], 0
	v_mfma_f32_16x16x32_f16 v[200:203], v[24:27], v[172:175], 0
	v_mfma_f32_16x16x32_f16 v[204:207], v[24:27], v[180:183], 0
	v_mfma_f32_16x16x32_f16 v[208:211], v[24:27], v[188:191], 0
	v_mfma_f32_16x16x32_f16 v[212:215], v[28:31], v[164:167], 0
	v_mfma_f32_16x16x32_f16 v[216:219], v[28:31], v[172:175], 0
	v_mfma_f32_16x16x32_f16 v[220:223], v[28:31], v[180:183], 0
	v_mfma_f32_16x16x32_f16 v[224:227], v[28:31], v[188:191], 0
	v_mfma_f32_16x16x32_f16 v[212:215], v[32:35], v[168:171], v[212:215]
	v_mfma_f32_16x16x32_f16 v[216:219], v[32:35], v[176:179], v[216:219]
	v_mfma_f32_16x16x32_f16 v[220:223], v[32:35], v[184:187], v[220:223]
	v_mfma_f32_16x16x32_f16 v[224:227], v[32:35], v[192:195], v[224:227]
	v_mul_f32_e32 v244, v196, v200
	v_mul_f32_e32 v250, v197, v201
	v_mul_f32_e32 v245, v200, v200
	v_mul_f32_e32 v251, v201, v201
	v_add_f32_e32 v246, v196, v200
	v_add_f32_e32 v252, v197, v201
	v_fma_f32 v245, v196, v196, v245
	v_fma_f32 v251, v197, v197, v251
	v_fma_f32 v247, v10, v246, v11
	v_fma_f32 v253, v10, v252, v11
	v_fma_f32 v246, v13, v208, v14
	v_fma_f32 v252, v13, v209, v14
	v_fma_f32 v248, v12, v204, v14
	v_fma_f32 v254, v12, v205, v14
	v_fma_f32 v249, 2.0, v244, v247
	v_fma_f32 v255, 2.0, v250, v253
	v_add_f32_e32 v247, v245, v247
	v_add_f32_e32 v253, v251, v253
	v_fma_f32 v246, -2.0, v244, v246
	v_fma_f32 v252, -2.0, v250, v252
	v_sub_f32_e32 v248, v248, v245
	v_sub_f32_e32 v254, v254, v251
	v_mul_f32_e32 v247, v247, v248
	v_mul_f32_e32 v253, v253, v254
	v_rcp_f32_e32 v247, v247
	v_rcp_f32_e32 v253, v253
	v_mul_f32_e32 v249, v249, v246
	v_mul_f32_e32 v255, v255, v252
	v_mul_f32_e32 v249, v249, v247
	v_mul_f32_e32 v255, v255, v253
	v_add_f32_e32 v21, v21, v249
	v_add_f32_e32 v21, v21, v255
	v_mul_f32_e32 v244, v198, v202
	v_mul_f32_e32 v250, v199, v203
	v_mul_f32_e32 v245, v202, v202
	v_mul_f32_e32 v251, v203, v203
	v_add_f32_e32 v246, v198, v202
	v_add_f32_e32 v252, v199, v203
	v_fma_f32 v245, v198, v198, v245
	v_fma_f32 v251, v199, v199, v251
	v_fma_f32 v247, v10, v246, v11
	v_fma_f32 v253, v10, v252, v11
	v_fma_f32 v246, v13, v210, v14
	v_fma_f32 v252, v13, v211, v14
	v_fma_f32 v248, v12, v206, v14
	v_fma_f32 v254, v12, v207, v14
	v_fma_f32 v249, 2.0, v244, v247
	v_fma_f32 v255, 2.0, v250, v253
	v_add_f32_e32 v247, v245, v247
	v_add_f32_e32 v253, v251, v253
	v_fma_f32 v246, -2.0, v244, v246
	v_fma_f32 v252, -2.0, v250, v252
	v_sub_f32_e32 v248, v248, v245
	v_sub_f32_e32 v254, v254, v251
	v_mul_f32_e32 v247, v247, v248
	v_mul_f32_e32 v253, v253, v254
	v_rcp_f32_e32 v247, v247
	v_rcp_f32_e32 v253, v253
	v_mul_f32_e32 v249, v249, v246
	v_mul_f32_e32 v255, v255, v252
	v_mul_f32_e32 v249, v249, v247
	v_mul_f32_e32 v255, v255, v253
	v_add_f32_e32 v22, v22, v249
	v_add_f32_e32 v22, v22, v255
	v_mfma_f32_16x16x32_f16 v[196:199], v[24:27], v[168:171], 0
	v_mfma_f32_16x16x32_f16 v[200:203], v[24:27], v[176:179], 0
	v_mfma_f32_16x16x32_f16 v[204:207], v[24:27], v[184:187], 0
	v_mfma_f32_16x16x32_f16 v[208:211], v[24:27], v[192:195], 0
	ds_read_b32 v23, v7 offset:96
	s_waitcnt lgkmcnt(0)
	v_cmp_ne_u32_e32 vcc, 0, v23
	s_cbranch_vccnz .Lq_go_3
.Lq_spin_3:
	s_sleep 1
	ds_read_b32 v23, v7 offset:96
	s_waitcnt lgkmcnt(0)
	v_cmp_eq_u32_e32 vcc, 0, v23
	s_cbranch_vccnz .Lq_spin_3
.Lq_go_3:
	ds_read_b128 v[228:231], v5 offset:49152
	ds_read_b128 v[232:235], v5 offset:49664
	ds_read_b128 v[236:239], v5 offset:50176
	ds_read_b128 v[240:243], v5 offset:50688
	v_mul_f32_e32 v244, v212, v216
	v_mul_f32_e32 v250, v213, v217
	v_mul_f32_e32 v245, v216, v216
	v_mul_f32_e32 v251, v217, v217
	v_add_f32_e32 v246, v212, v216
	v_add_f32_e32 v252, v213, v217
	v_fma_f32 v245, v212, v212, v245
	v_fma_f32 v251, v213, v213, v251
	v_fma_f32 v247, v10, v246, v11
	v_fma_f32 v253, v10, v252, v11
	v_fma_f32 v246, v13, v224, v14
	v_fma_f32 v252, v13, v225, v14
	v_fma_f32 v248, v12, v220, v14
	v_fma_f32 v254, v12, v221, v14
	v_fma_f32 v249, 2.0, v244, v247
	v_fma_f32 v255, 2.0, v250, v253
	v_add_f32_e32 v247, v245, v247
	v_add_f32_e32 v253, v251, v253
	v_fma_f32 v246, -2.0, v244, v246
	v_fma_f32 v252, -2.0, v250, v252
	v_sub_f32_e32 v248, v248, v245
	v_sub_f32_e32 v254, v254, v251
	v_mul_f32_e32 v247, v247, v248
	v_mul_f32_e32 v253, v253, v254
	v_rcp_f32_e32 v247, v247
	v_rcp_f32_e32 v253, v253
	v_mul_f32_e32 v249, v249, v246
	v_mul_f32_e32 v255, v255, v252
	v_mul_f32_e32 v249, v249, v247
	v_mul_f32_e32 v255, v255, v253
	v_add_f32_e32 v21, v21, v249
	v_add_f32_e32 v21, v21, v255
	v_mul_f32_e32 v244, v214, v218
	v_mul_f32_e32 v250, v215, v219
	v_mul_f32_e32 v245, v218, v218
	v_mul_f32_e32 v251, v219, v219
	v_add_f32_e32 v246, v214, v218
	v_add_f32_e32 v252, v215, v219
	v_fma_f32 v245, v214, v214, v245
	v_fma_f32 v251, v215, v215, v251
	v_fma_f32 v247, v10, v246, v11
	v_fma_f32 v253, v10, v252, v11
	v_fma_f32 v246, v13, v226, v14
	v_fma_f32 v252, v13, v227, v14
	v_fma_f32 v248, v12, v222, v14
	v_fma_f32 v254, v12, v223, v14
	v_fma_f32 v249, 2.0, v244, v247
	v_fma_f32 v255, 2.0, v250, v253
	v_add_f32_e32 v247, v245, v247
	v_add_f32_e32 v253, v251, v253
	v_fma_f32 v246, -2.0, v244, v246
	v_fma_f32 v252, -2.0, v250, v252
	v_sub_f32_e32 v248, v248, v245
	v_sub_f32_e32 v254, v254, v251
	v_mul_f32_e32 v247, v247, v248
	v_mul_f32_e32 v253, v253, v254
	v_rcp_f32_e32 v247, v247
	v_rcp_f32_e32 v253, v253
	v_mul_f32_e32 v249, v249, v246
	v_mul_f32_e32 v255, v255, v252
	v_mul_f32_e32 v249, v249, v247
	v_mul_f32_e32 v255, v255, v253
	v_add_f32_e32 v22, v22, v249
	v_add_f32_e32 v22, v22, v255
	s_waitcnt lgkmcnt(0)
	v_mfma_f32_16x16x32_f16 v[212:215], v[28:31], v[228:231], 0
	v_mfma_f32_16x16x32_f16 v[216:219], v[28:31], v[232:235], 0
	v_mfma_f32_16x16x32_f16 v[220:223], v[28:31], v[236:239], 0
	v_mfma_f32_16x16x32_f16 v[224:227], v[28:31], v[240:243], 0
	v_mfma_f32_16x16x32_f16 v[212:215], v[32:35], v[164:167], v[212:215]
	v_mfma_f32_16x16x32_f16 v[216:219], v[32:35], v[172:175], v[216:219]
	v_mfma_f32_16x16x32_f16 v[220:223], v[32:35], v[180:183], v[220:223]
	v_mfma_f32_16x16x32_f16 v[224:227], v[32:35], v[188:191], v[224:227]
	v_mul_f32_e32 v244, v196, v200
	v_mul_f32_e32 v250, v197, v201
	v_mul_f32_e32 v245, v200, v200
	v_mul_f32_e32 v251, v201, v201
	v_add_f32_e32 v246, v196, v200
	v_add_f32_e32 v252, v197, v201
	v_fma_f32 v245, v196, v196, v245
	v_fma_f32 v251, v197, v197, v251
	v_fma_f32 v247, v10, v246, v11
	v_fma_f32 v253, v10, v252, v11
	v_fma_f32 v246, v13, v208, v14
	v_fma_f32 v252, v13, v209, v14
	v_fma_f32 v248, v12, v204, v14
	v_fma_f32 v254, v12, v205, v14
	v_fma_f32 v249, 2.0, v244, v247
	v_fma_f32 v255, 2.0, v250, v253
	v_add_f32_e32 v247, v245, v247
	v_add_f32_e32 v253, v251, v253
	v_fma_f32 v246, -2.0, v244, v246
	v_fma_f32 v252, -2.0, v250, v252
	v_sub_f32_e32 v248, v248, v245
	v_sub_f32_e32 v254, v254, v251
	v_mul_f32_e32 v247, v247, v248
	v_mul_f32_e32 v253, v253, v254
	v_rcp_f32_e32 v247, v247
	v_rcp_f32_e32 v253, v253
	v_mul_f32_e32 v249, v249, v246
	v_mul_f32_e32 v255, v255, v252
	v_mul_f32_e32 v249, v249, v247
	v_mul_f32_e32 v255, v255, v253
	v_add_f32_e32 v21, v21, v249
	v_add_f32_e32 v21, v21, v255
	v_mul_f32_e32 v244, v198, v202
	v_mul_f32_e32 v250, v199, v203
	v_mul_f32_e32 v245, v202, v202
	v_mul_f32_e32 v251, v203, v203
	v_add_f32_e32 v246, v198, v202
	v_add_f32_e32 v252, v199, v203
	v_fma_f32 v245, v198, v198, v245
	v_fma_f32 v251, v199, v199, v251
	v_fma_f32 v247, v10, v246, v11
	v_fma_f32 v253, v10, v252, v11
	v_fma_f32 v246, v13, v210, v14
	v_fma_f32 v252, v13, v211, v14
	v_fma_f32 v248, v12, v206, v14
	v_fma_f32 v254, v12, v207, v14
	v_fma_f32 v249, 2.0, v244, v247
	v_fma_f32 v255, 2.0, v250, v253
	v_add_f32_e32 v247, v245, v247
	v_add_f32_e32 v253, v251, v253
	v_fma_f32 v246, -2.0, v244, v246
	v_fma_f32 v252, -2.0, v250, v252
	v_sub_f32_e32 v248, v248, v245
	v_sub_f32_e32 v254, v254, v251
	v_mul_f32_e32 v247, v247, v248
	v_mul_f32_e32 v253, v253, v254
	v_rcp_f32_e32 v247, v247
	v_rcp_f32_e32 v253, v253
	v_mul_f32_e32 v249, v249, v246
	v_mul_f32_e32 v255, v255, v252
	v_mul_f32_e32 v249, v249, v247
	v_mul_f32_e32 v255, v255, v253
	v_add_f32_e32 v22, v22, v249
	v_add_f32_e32 v22, v22, v255
	v_mul_f32_e32 v244, v212, v216
	v_mul_f32_e32 v250, v213, v217
	v_mul_f32_e32 v245, v216, v216
	v_mul_f32_e32 v251, v217, v217
	v_add_f32_e32 v246, v212, v216
	v_add_f32_e32 v252, v213, v217
	v_fma_f32 v245, v212, v212, v245
	v_fma_f32 v251, v213, v213, v251
	v_fma_f32 v247, v10, v246, v11
	v_fma_f32 v253, v10, v252, v11
	v_fma_f32 v246, v13, v224, v14
	v_fma_f32 v252, v13, v225, v14
	v_fma_f32 v248, v12, v220, v14
	v_fma_f32 v254, v12, v221, v14
	v_fma_f32 v249, 2.0, v244, v247
	v_fma_f32 v255, 2.0, v250, v253
	v_add_f32_e32 v247, v245, v247
	v_add_f32_e32 v253, v251, v253
	v_fma_f32 v246, -2.0, v244, v246
	v_fma_f32 v252, -2.0, v250, v252
	v_sub_f32_e32 v248, v248, v245
	v_sub_f32_e32 v254, v254, v251
	v_mul_f32_e32 v247, v247, v248
	v_mul_f32_e32 v253, v253, v254
	v_rcp_f32_e32 v247, v247
	v_rcp_f32_e32 v253, v253
	v_mul_f32_e32 v249, v249, v246
	v_mul_f32_e32 v255, v255, v252
	v_mul_f32_e32 v249, v249, v247
	v_mul_f32_e32 v255, v255, v253
	v_fma_f32 v21, v249, v15, v21
	v_fma_f32 v21, v255, v16, v21
	v_mul_f32_e32 v244, v214, v218
	v_mul_f32_e32 v250, v215, v219
	v_mul_f32_e32 v245, v218, v218
	v_mul_f32_e32 v251, v219, v219
	v_add_f32_e32 v246, v214, v218
	v_add_f32_e32 v252, v215, v219
	v_fma_f32 v245, v214, v214, v245
	v_fma_f32 v251, v215, v215, v251
	v_fma_f32 v247, v10, v246, v11
	v_fma_f32 v253, v10, v252, v11
	v_fma_f32 v246, v13, v226, v14
	v_fma_f32 v252, v13, v227, v14
	v_fma_f32 v248, v12, v222, v14
	v_fma_f32 v254, v12, v223, v14
	v_fma_f32 v249, 2.0, v244, v247
	v_fma_f32 v255, 2.0, v250, v253
	v_add_f32_e32 v247, v245, v247
	v_add_f32_e32 v253, v251, v253
	v_fma_f32 v246, -2.0, v244, v246
	v_fma_f32 v252, -2.0, v250, v252
	v_sub_f32_e32 v248, v248, v245
	v_sub_f32_e32 v254, v254, v251
	v_mul_f32_e32 v247, v247, v248
	v_mul_f32_e32 v253, v253, v254
	v_rcp_f32_e32 v247, v247
	v_rcp_f32_e32 v253, v253
	v_mul_f32_e32 v249, v249, v246
	v_mul_f32_e32 v255, v255, v252
	v_mul_f32_e32 v249, v249, v247
	v_mul_f32_e32 v255, v255, v253
	v_fma_f32 v22, v249, v17, v22
	v_fma_f32 v22, v255, v18, v22
	v_add_f32_e32 v19, v19, v20
	v_add_f32_e32 v21, v21, v22
	s_cmp_eq_u32 s15, 7
	s_cselect_b32 s23, 6, 16
	v_cmp_gt_u32_e32 vcc, s23, v9
	s_nop 1
	v_cndmask_b32_e32 v21, 0, v21, vcc
	v_add_f32_e32 v19, v19, v21
	v_lshlrev_b32_e32 v23, 2, v1
	v_xor_b32_e32 v20, 128, v23
	ds_bpermute_b32 v22, v20, v19
	s_waitcnt lgkmcnt(0)
	v_add_f32_e32 v19, v19, v22
	v_xor_b32_e32 v20, 64, v23
	ds_bpermute_b32 v22, v20, v19
	s_waitcnt lgkmcnt(0)
	v_add_f32_e32 v19, v19, v22
	v_xor_b32_e32 v20, 32, v23
	ds_bpermute_b32 v22, v20, v19
	s_waitcnt lgkmcnt(0)
	v_add_f32_e32 v19, v19, v22
	v_xor_b32_e32 v20, 16, v23
	ds_bpermute_b32 v22, v20, v19
	s_waitcnt lgkmcnt(0)
	v_add_f32_e32 v19, v19, v22
	v_xor_b32_e32 v20, 8, v23
	ds_bpermute_b32 v22, v20, v19
	s_waitcnt lgkmcnt(0)
	v_add_f32_e32 v19, v19, v22
	v_xor_b32_e32 v20, 4, v23
	ds_bpermute_b32 v22, v20, v19
	s_waitcnt lgkmcnt(0)
	v_add_f32_e32 v19, v19, v22
	v_cmp_eq_u32_e32 vcc, 0, v1
	s_nop 1
	s_and_saveexec_b64 s[30:31], vcc
	s_lshl_b32 s24, s2, 3
	s_add_u32 s24, s24, s12
	s_lshl_b32 s24, s24, 2
	v_mov_b32_e32 v23, s24
	global_store_dword v23, v19, s[10:11]
	s_endpgm

	.amdhsa_kernel _Z9ssim_mainPKfS0_S0_Pf
		.amdhsa_group_segment_fixed_size 145536
		.amdhsa_private_segment_fixed_size 0
		.amdhsa_kernarg_size 32
		.amdhsa_user_sgpr_count 2
		.amdhsa_user_sgpr_dispatch_ptr 0
		.amdhsa_user_sgpr_queue_ptr 0
		.amdhsa_user_sgpr_kernarg_segment_ptr 1
		.amdhsa_user_sgpr_dispatch_id 0
		.amdhsa_user_sgpr_kernarg_preload_length 0
		.amdhsa_user_sgpr_kernarg_preload_offset 0
		.amdhsa_user_sgpr_private_segment_size 0
		.amdhsa_uses_dynamic_stack 0
		.amdhsa_enable_private_segment 0
		.amdhsa_system_sgpr_workgroup_id_x 1
		.amdhsa_system_sgpr_workgroup_id_y 0
		.amdhsa_system_sgpr_workgroup_id_z 0
		.amdhsa_system_sgpr_workgroup_info 0
		.amdhsa_system_vgpr_workitem_id 0
		.amdhsa_next_free_vgpr 256
		.amdhsa_next_free_sgpr 96
		.amdhsa_accum_offset 256
		.amdhsa_reserve_vcc 1
		.amdhsa_float_round_mode_32 0
		.amdhsa_float_round_mode_16_64 0
		.amdhsa_float_denorm_mode_32 3
		.amdhsa_float_denorm_mode_16_64 3
		.amdhsa_dx10_clamp 1
		.amdhsa_ieee_mode 1
		.amdhsa_fp16_overflow 0
		.amdhsa_tg_split 0
		.amdhsa_exception_fp_ieee_invalid_op 0
		.amdhsa_exception_fp_denorm_src 0
		.amdhsa_exception_fp_ieee_div_zero 0
		.amdhsa_exception_fp_ieee_overflow 0
		.amdhsa_exception_fp_ieee_underflow 0
		.amdhsa_exception_fp_ieee_inexact 0
		.amdhsa_exception_int_div_zero 0
	.end_amdhsa_kernel

amdhsa.kernels:
  - .agpr_count:     0
    .args:
      - .actual_access:  read_only
        .address_space:  global
        .offset:         0
        .size:           8
        .value_kind:     global_buffer
      - .actual_access:  read_only
        .address_space:  global
        .offset:         8
        .size:           8
        .value_kind:     global_buffer
      - .actual_access:  read_only
        .address_space:  global
        .offset:         16
        .size:           8
        .value_kind:     global_buffer
      - .actual_access:  write_only
        .address_space:  global
        .offset:         24
        .size:           8
        .value_kind:     global_buffer
    .group_segment_fixed_size: 145536
    .kernarg_segment_align: 8
    .kernarg_segment_size: 32
    .language:       OpenCL C
    .language_version:
      - 2
      - 0
    .max_flat_workgroup_size: 512
    .name:           _Z9ssim_mainPKfS0_S0_Pf
    .private_segment_fixed_size: 0
    .sgpr_count:     37
    .sgpr_spill_count: 0
    .symbol:         _Z9ssim_mainPKfS0_S0_Pf.kd
    .uniform_work_group_size: 1
    .uses_dynamic_stack: false
    .vgpr_count:     256
    .vgpr_spill_count: 0
    .wavefront_size: 64
  - .agpr_count:     0
    .args:
      - .actual_access:  read_only
        .address_space:  global
        .offset:         0
        .size:           8
        .value_kind:     global_buffer
      - .actual_access:  write_only
        .address_space:  global
        .offset:         8
        .size:           8
        .value_kind:     global_buffer
    .group_segment_fixed_size: 0
    .kernarg_segment_align: 8
    .kernarg_segment_size: 16
    .language:       OpenCL C
    .language_version:
      - 2
      - 0
    .max_flat_workgroup_size: 64
    .name:           _Z10ssim_finalPKfPf
    .private_segment_fixed_size: 0
    .sgpr_count:     12
    .sgpr_spill_count: 0
    .symbol:         _Z10ssim_finalPKfPf.kd
    .uniform_work_group_size: 1
    .uses_dynamic_stack: false
    .vgpr_count:     53
    .vgpr_spill_count: 0
    .wavefront_size: 64
